# norm2: next pass's x/delta rows touched (plain loads to scratch regs) from the middle of the router section so the pass-top loads hit L2
# baseline (speedup 1.0000x reference)
; #define LAS __attribute__((address_space(3)))
; __device__ __forceinline__ void phase_norm2(const Params& p, const Ctx& F, const int l) {
;     ...
;         f32x2 lg[16];
;         unsigned wro = (unsigned)(uintptr_t)wr; asm volatile("" : "+v"(wro));
;         const LAS float* wr2 = (const LAS float*)(uintptr_t)wro;
; #pragma unroll
;         for (int e = 0; e < 16; ++e) { f32x2 a = {0.f, 0.f};
; #pragma unroll
;             for (int j = 0; j < 8; ++j) { const f32x4 w = *((const LAS f32x4*)(wr2 + e * DM) + F.lane + 64 * j);
; #pragma unroll
;                 for (int c = 0; c < 4; ++c) a += vv[j][c] * w[c]; }
;             lg[e] = a; }
.LBB0_937:
	s_or_b64 exec, exec, s[12:13]
	v_mov_b32_e32 v1, v35
	s_nop 0
	v_lshl_add_u32 v182, v132, 4, v1
	v_add_u32_e32 v244, 0x10000, v182
	ds_read_b128 v[224:227], v182
	ds_read_b128 v[228:231], v182 offset:1024
	ds_read_b128 v[232:235], v182 offset:2048
	ds_read_b128 v[236:239], v182 offset:3072
	s_waitcnt lgkmcnt(3)
	v_pk_fma_f32 v[156:157], v[124:125], v[224:225], 0 op_sel_hi:[1,0,0]
	s_nop 0
	v_pk_fma_f32 v[152:153], v[126:127], v[224:225], v[156:157] op_sel:[0,1,0]
	s_nop 0
	v_pk_fma_f32 v[152:153], v[128:129], v[226:227], v[152:153] op_sel_hi:[1,0,1]
	v_mov_b32_e32 v154, v227
	v_pk_fma_f32 v[156:157], v[130:131], v[154:155], v[152:153] op_sel_hi:[1,0,1]
	ds_read_b128 v[240:243], v182 offset:4096
	s_waitcnt lgkmcnt(3)
	v_pk_fma_f32 v[156:157], v[112:113], v[228:229], v[156:157] op_sel_hi:[1,0,1]
	s_nop 0
	v_pk_fma_f32 v[152:153], v[114:115], v[228:229], v[156:157] op_sel:[0,1,0]
	s_nop 0
	v_pk_fma_f32 v[152:153], v[118:119], v[230:231], v[152:153] op_sel_hi:[1,0,1]
	v_mov_b32_e32 v154, v231
	v_pk_fma_f32 v[156:157], v[122:123], v[154:155], v[152:153] op_sel_hi:[1,0,1]
	ds_read_b128 v[224:227], v182 offset:5120
	s_waitcnt lgkmcnt(3)
	v_pk_fma_f32 v[156:157], v[108:109], v[232:233], v[156:157] op_sel_hi:[1,0,1]
	s_nop 0
	v_pk_fma_f32 v[152:153], v[110:111], v[232:233], v[156:157] op_sel:[0,1,0]
	s_nop 0
	v_pk_fma_f32 v[152:153], v[116:117], v[234:235], v[152:153] op_sel_hi:[1,0,1]
	v_mov_b32_e32 v154, v235
	v_pk_fma_f32 v[156:157], v[120:121], v[154:155], v[152:153] op_sel_hi:[1,0,1]
	ds_read_b128 v[228:231], v182 offset:6144
	s_waitcnt lgkmcnt(3)
	v_pk_fma_f32 v[156:157], v[96:97], v[236:237], v[156:157] op_sel_hi:[1,0,1]
	s_nop 0
	v_pk_fma_f32 v[152:153], v[98:99], v[236:237], v[156:157] op_sel:[0,1,0]
	s_nop 0
	v_pk_fma_f32 v[152:153], v[102:103], v[238:239], v[152:153] op_sel_hi:[1,0,1]
	v_mov_b32_e32 v154, v239
	v_pk_fma_f32 v[156:157], v[106:107], v[154:155], v[152:153] op_sel_hi:[1,0,1]
	ds_read_b128 v[232:235], v182 offset:7168
	s_waitcnt lgkmcnt(3)
	v_pk_fma_f32 v[156:157], v[92:93], v[240:241], v[156:157] op_sel_hi:[1,0,1]
	s_nop 0
	v_pk_fma_f32 v[152:153], v[94:95], v[240:241], v[156:157] op_sel:[0,1,0]
	s_nop 0
	v_pk_fma_f32 v[152:153], v[100:101], v[242:243], v[152:153] op_sel_hi:[1,0,1]
	v_mov_b32_e32 v154, v243
	v_pk_fma_f32 v[156:157], v[104:105], v[154:155], v[152:153] op_sel_hi:[1,0,1]
	ds_read_b128 v[236:239], v182 offset:8192
	s_waitcnt lgkmcnt(3)
	v_pk_fma_f32 v[156:157], v[80:81], v[224:225], v[156:157] op_sel_hi:[1,0,1]
	s_nop 0
	v_pk_fma_f32 v[152:153], v[82:83], v[224:225], v[156:157] op_sel:[0,1,0]
	s_nop 0
	v_pk_fma_f32 v[152:153], v[86:87], v[226:227], v[152:153] op_sel_hi:[1,0,1]
	v_mov_b32_e32 v154, v227
	v_pk_fma_f32 v[156:157], v[90:91], v[154:155], v[152:153] op_sel_hi:[1,0,1]
	ds_read_b128 v[240:243], v182 offset:9216
	s_waitcnt lgkmcnt(3)
	v_pk_fma_f32 v[156:157], v[76:77], v[228:229], v[156:157] op_sel_hi:[1,0,1]
	s_nop 0
	v_pk_fma_f32 v[152:153], v[78:79], v[228:229], v[156:157] op_sel:[0,1,0]
	s_nop 0
	v_pk_fma_f32 v[152:153], v[84:85], v[230:231], v[152:153] op_sel_hi:[1,0,1]
	v_mov_b32_e32 v154, v231
	v_pk_fma_f32 v[156:157], v[88:89], v[154:155], v[152:153] op_sel_hi:[1,0,1]
	ds_read_b128 v[224:227], v182 offset:10240
	s_waitcnt lgkmcnt(3)
	v_pk_fma_f32 v[156:157], v[68:69], v[232:233], v[156:157] op_sel_hi:[1,0,1]
	s_nop 0
	v_pk_fma_f32 v[152:153], v[70:71], v[232:233], v[156:157] op_sel:[0,1,0]
	s_nop 0
	v_pk_fma_f32 v[152:153], v[72:73], v[234:235], v[152:153] op_sel_hi:[1,0,1]
	v_mov_b32_e32 v154, v235
	v_pk_fma_f32 v[152:153], v[74:75], v[154:155], v[152:153] op_sel_hi:[1,0,1]
	ds_read_b128 v[228:231], v182 offset:11264
	s_waitcnt lgkmcnt(3)
	v_pk_fma_f32 v[158:159], v[124:125], v[236:237], 0 op_sel_hi:[1,0,0]
	s_nop 0
	v_pk_fma_f32 v[154:155], v[126:127], v[236:237], v[158:159] op_sel:[0,1,0]
	s_nop 0
	v_pk_fma_f32 v[154:155], v[128:129], v[238:239], v[154:155] op_sel_hi:[1,0,1]
	v_mov_b32_e32 v156, v239
	v_pk_fma_f32 v[158:159], v[130:131], v[156:157], v[154:155] op_sel_hi:[1,0,1]
	ds_read_b128 v[232:235], v182 offset:12288
	s_waitcnt lgkmcnt(3)
	v_pk_fma_f32 v[158:159], v[112:113], v[240:241], v[158:159] op_sel_hi:[1,0,1]
	s_nop 0
	v_pk_fma_f32 v[154:155], v[114:115], v[240:241], v[158:159] op_sel:[0,1,0]
	s_nop 0
	v_pk_fma_f32 v[154:155], v[118:119], v[242:243], v[154:155] op_sel_hi:[1,0,1]
	v_mov_b32_e32 v156, v243
	v_pk_fma_f32 v[158:159], v[122:123], v[156:157], v[154:155] op_sel_hi:[1,0,1]
	ds_read_b128 v[236:239], v182 offset:13312
	s_waitcnt lgkmcnt(3)
	v_pk_fma_f32 v[158:159], v[108:109], v[224:225], v[158:159] op_sel_hi:[1,0,1]
	s_nop 0
	v_pk_fma_f32 v[154:155], v[110:111], v[224:225], v[158:159] op_sel:[0,1,0]
	s_nop 0
	v_pk_fma_f32 v[154:155], v[116:117], v[226:227], v[154:155] op_sel_hi:[1,0,1]
	v_mov_b32_e32 v156, v227
	v_pk_fma_f32 v[158:159], v[120:121], v[156:157], v[154:155] op_sel_hi:[1,0,1]
	ds_read_b128 v[240:243], v182 offset:14336
	s_waitcnt lgkmcnt(3)
	v_pk_fma_f32 v[158:159], v[96:97], v[228:229], v[158:159] op_sel_hi:[1,0,1]
	s_nop 0
	v_pk_fma_f32 v[154:155], v[98:99], v[228:229], v[158:159] op_sel:[0,1,0]
	s_nop 0
	v_pk_fma_f32 v[154:155], v[102:103], v[230:231], v[154:155] op_sel_hi:[1,0,1]
	v_mov_b32_e32 v156, v231
	v_pk_fma_f32 v[158:159], v[106:107], v[156:157], v[154:155] op_sel_hi:[1,0,1]
	ds_read_b128 v[224:227], v182 offset:15360
	s_waitcnt lgkmcnt(3)
	v_pk_fma_f32 v[158:159], v[92:93], v[232:233], v[158:159] op_sel_hi:[1,0,1]
	s_nop 0
	v_pk_fma_f32 v[154:155], v[94:95], v[232:233], v[158:159] op_sel:[0,1,0]
	s_nop 0
	v_pk_fma_f32 v[154:155], v[100:101], v[234:235], v[154:155] op_sel_hi:[1,0,1]
	v_mov_b32_e32 v156, v235
	v_pk_fma_f32 v[158:159], v[104:105], v[156:157], v[154:155] op_sel_hi:[1,0,1]
	ds_read_b128 v[228:231], v182 offset:16384
	s_waitcnt lgkmcnt(3)
; #define LAS __attribute__((address_space(3)))
; __device__ __forceinline__ void phase_norm2(const Params& p, const Ctx& F, const int l) {
;     ...
; #pragma unroll
;         for (int e = 0; e < 16; ++e) { f32x2 a = {0.f, 0.f};
; #pragma unroll
;             for (int j = 0; j < 8; ++j) { const f32x4 w = *((const LAS f32x4*)(wr2 + e * DM) + F.lane + 64 * j);
; #pragma unroll
;                 for (int c = 0; c < 4; ++c) a += vv[j][c] * w[c]; }
;             lg[e] = a; }
	v_pk_fma_f32 v[158:159], v[80:81], v[236:237], v[158:159] op_sel_hi:[1,0,1]
	s_nop 0
	v_pk_fma_f32 v[154:155], v[82:83], v[236:237], v[158:159] op_sel:[0,1,0]
	s_nop 0
	v_pk_fma_f32 v[154:155], v[86:87], v[238:239], v[154:155] op_sel_hi:[1,0,1]
	v_mov_b32_e32 v156, v239
	v_pk_fma_f32 v[158:159], v[90:91], v[156:157], v[154:155] op_sel_hi:[1,0,1]
	ds_read_b128 v[232:235], v182 offset:17408
	s_waitcnt lgkmcnt(3)
	v_pk_fma_f32 v[158:159], v[76:77], v[240:241], v[158:159] op_sel_hi:[1,0,1]
	s_nop 0
	v_pk_fma_f32 v[154:155], v[78:79], v[240:241], v[158:159] op_sel:[0,1,0]
	s_nop 0
	v_pk_fma_f32 v[154:155], v[84:85], v[242:243], v[154:155] op_sel_hi:[1,0,1]
	v_mov_b32_e32 v156, v243
	v_pk_fma_f32 v[158:159], v[88:89], v[156:157], v[154:155] op_sel_hi:[1,0,1]
	ds_read_b128 v[236:239], v182 offset:18432
	s_waitcnt lgkmcnt(3)
	v_pk_fma_f32 v[158:159], v[68:69], v[224:225], v[158:159] op_sel_hi:[1,0,1]
	s_nop 0
	v_pk_fma_f32 v[154:155], v[70:71], v[224:225], v[158:159] op_sel:[0,1,0]
	s_nop 0
	v_pk_fma_f32 v[154:155], v[72:73], v[226:227], v[154:155] op_sel_hi:[1,0,1]
	v_mov_b32_e32 v156, v227
	v_pk_fma_f32 v[154:155], v[74:75], v[156:157], v[154:155] op_sel_hi:[1,0,1]
	ds_read_b128 v[240:243], v182 offset:19456
	s_waitcnt lgkmcnt(3)
	v_pk_fma_f32 v[160:161], v[124:125], v[228:229], 0 op_sel_hi:[1,0,0]
	s_nop 0
	v_pk_fma_f32 v[156:157], v[126:127], v[228:229], v[160:161] op_sel:[0,1,0]
	s_nop 0
	v_pk_fma_f32 v[156:157], v[128:129], v[230:231], v[156:157] op_sel_hi:[1,0,1]
	v_mov_b32_e32 v158, v231
	v_pk_fma_f32 v[160:161], v[130:131], v[158:159], v[156:157] op_sel_hi:[1,0,1]
	ds_read_b128 v[224:227], v182 offset:20480
	s_waitcnt lgkmcnt(3)
	v_pk_fma_f32 v[160:161], v[112:113], v[232:233], v[160:161] op_sel_hi:[1,0,1]
	s_nop 0
	v_pk_fma_f32 v[156:157], v[114:115], v[232:233], v[160:161] op_sel:[0,1,0]
	s_nop 0
	v_pk_fma_f32 v[156:157], v[118:119], v[234:235], v[156:157] op_sel_hi:[1,0,1]
	v_mov_b32_e32 v158, v235
	v_pk_fma_f32 v[160:161], v[122:123], v[158:159], v[156:157] op_sel_hi:[1,0,1]
	ds_read_b128 v[228:231], v182 offset:21504
	s_waitcnt lgkmcnt(3)
	v_pk_fma_f32 v[160:161], v[108:109], v[236:237], v[160:161] op_sel_hi:[1,0,1]
	s_nop 0
	v_pk_fma_f32 v[156:157], v[110:111], v[236:237], v[160:161] op_sel:[0,1,0]
	s_nop 0
	v_pk_fma_f32 v[156:157], v[116:117], v[238:239], v[156:157] op_sel_hi:[1,0,1]
	v_mov_b32_e32 v158, v239
	v_pk_fma_f32 v[160:161], v[120:121], v[158:159], v[156:157] op_sel_hi:[1,0,1]
	ds_read_b128 v[232:235], v182 offset:22528
	s_waitcnt lgkmcnt(3)
	v_pk_fma_f32 v[160:161], v[96:97], v[240:241], v[160:161] op_sel_hi:[1,0,1]
	s_nop 0
	v_pk_fma_f32 v[156:157], v[98:99], v[240:241], v[160:161] op_sel:[0,1,0]
	s_nop 0
	v_pk_fma_f32 v[156:157], v[102:103], v[242:243], v[156:157] op_sel_hi:[1,0,1]
	v_mov_b32_e32 v158, v243
	v_pk_fma_f32 v[160:161], v[106:107], v[158:159], v[156:157] op_sel_hi:[1,0,1]
	ds_read_b128 v[236:239], v182 offset:23552
	s_waitcnt lgkmcnt(3)
	v_pk_fma_f32 v[160:161], v[92:93], v[224:225], v[160:161] op_sel_hi:[1,0,1]
	s_nop 0
	v_pk_fma_f32 v[156:157], v[94:95], v[224:225], v[160:161] op_sel:[0,1,0]
	s_nop 0
	v_pk_fma_f32 v[156:157], v[100:101], v[226:227], v[156:157] op_sel_hi:[1,0,1]
	v_mov_b32_e32 v158, v227
	v_pk_fma_f32 v[160:161], v[104:105], v[158:159], v[156:157] op_sel_hi:[1,0,1]
	ds_read_b128 v[240:243], v182 offset:24576
	s_waitcnt lgkmcnt(3)
	v_pk_fma_f32 v[160:161], v[80:81], v[228:229], v[160:161] op_sel_hi:[1,0,1]
	s_nop 0
	v_pk_fma_f32 v[156:157], v[82:83], v[228:229], v[160:161] op_sel:[0,1,0]
	s_nop 0
	v_pk_fma_f32 v[156:157], v[86:87], v[230:231], v[156:157] op_sel_hi:[1,0,1]
	v_mov_b32_e32 v158, v231
	v_pk_fma_f32 v[160:161], v[90:91], v[158:159], v[156:157] op_sel_hi:[1,0,1]
	ds_read_b128 v[224:227], v182 offset:25600
	s_waitcnt lgkmcnt(3)
	v_pk_fma_f32 v[160:161], v[76:77], v[232:233], v[160:161] op_sel_hi:[1,0,1]
	s_nop 0
	v_pk_fma_f32 v[156:157], v[78:79], v[232:233], v[160:161] op_sel:[0,1,0]
	s_nop 0
	v_pk_fma_f32 v[156:157], v[84:85], v[234:235], v[156:157] op_sel_hi:[1,0,1]
	v_mov_b32_e32 v158, v235
	v_pk_fma_f32 v[160:161], v[88:89], v[158:159], v[156:157] op_sel_hi:[1,0,1]
	ds_read_b128 v[228:231], v182 offset:26624
	s_waitcnt lgkmcnt(3)
	v_pk_fma_f32 v[160:161], v[68:69], v[236:237], v[160:161] op_sel_hi:[1,0,1]
	s_nop 0
	v_pk_fma_f32 v[156:157], v[70:71], v[236:237], v[160:161] op_sel:[0,1,0]
	s_nop 0
	v_pk_fma_f32 v[156:157], v[72:73], v[238:239], v[156:157] op_sel_hi:[1,0,1]
	v_mov_b32_e32 v158, v239
	v_pk_fma_f32 v[156:157], v[74:75], v[158:159], v[156:157] op_sel_hi:[1,0,1]
	ds_read_b128 v[232:235], v182 offset:27648
	s_waitcnt lgkmcnt(3)
	v_pk_fma_f32 v[162:163], v[124:125], v[240:241], 0 op_sel_hi:[1,0,0]
	s_nop 0
	v_pk_fma_f32 v[158:159], v[126:127], v[240:241], v[162:163] op_sel:[0,1,0]
	s_nop 0
	v_pk_fma_f32 v[158:159], v[128:129], v[242:243], v[158:159] op_sel_hi:[1,0,1]
	v_mov_b32_e32 v160, v243
	v_pk_fma_f32 v[162:163], v[130:131], v[160:161], v[158:159] op_sel_hi:[1,0,1]
	ds_read_b128 v[236:239], v182 offset:28672
	s_waitcnt lgkmcnt(3)
	v_pk_fma_f32 v[162:163], v[112:113], v[224:225], v[162:163] op_sel_hi:[1,0,1]
	s_nop 0
	v_pk_fma_f32 v[158:159], v[114:115], v[224:225], v[162:163] op_sel:[0,1,0]
	s_nop 0
	v_pk_fma_f32 v[158:159], v[118:119], v[226:227], v[158:159] op_sel_hi:[1,0,1]
	v_mov_b32_e32 v160, v227
	v_pk_fma_f32 v[162:163], v[122:123], v[160:161], v[158:159] op_sel_hi:[1,0,1]
	ds_read_b128 v[240:243], v182 offset:29696
	s_waitcnt lgkmcnt(3)
	v_pk_fma_f32 v[162:163], v[108:109], v[228:229], v[162:163] op_sel_hi:[1,0,1]
	s_nop 0
	v_pk_fma_f32 v[158:159], v[110:111], v[228:229], v[162:163] op_sel:[0,1,0]
	s_nop 0
	v_pk_fma_f32 v[158:159], v[116:117], v[230:231], v[158:159] op_sel_hi:[1,0,1]
	v_mov_b32_e32 v160, v231
	v_pk_fma_f32 v[162:163], v[120:121], v[160:161], v[158:159] op_sel_hi:[1,0,1]
	ds_read_b128 v[224:227], v182 offset:30720
	s_waitcnt lgkmcnt(3)
; #define LAS __attribute__((address_space(3)))
; __device__ __forceinline__ void phase_norm2(const Params& p, const Ctx& F, const int l) {
;     ...
; #pragma unroll
;         for (int e = 0; e < 16; ++e) { f32x2 a = {0.f, 0.f};
; #pragma unroll
;             for (int j = 0; j < 8; ++j) { const f32x4 w = *((const LAS f32x4*)(wr2 + e * DM) + F.lane + 64 * j);
; #pragma unroll
;                 for (int c = 0; c < 4; ++c) a += vv[j][c] * w[c]; }
;             lg[e] = a; }
	v_pk_fma_f32 v[162:163], v[96:97], v[232:233], v[162:163] op_sel_hi:[1,0,1]
	s_nop 0
	v_pk_fma_f32 v[158:159], v[98:99], v[232:233], v[162:163] op_sel:[0,1,0]
	s_nop 0
	v_pk_fma_f32 v[158:159], v[102:103], v[234:235], v[158:159] op_sel_hi:[1,0,1]
	v_mov_b32_e32 v160, v235
	v_pk_fma_f32 v[162:163], v[106:107], v[160:161], v[158:159] op_sel_hi:[1,0,1]
	ds_read_b128 v[228:231], v182 offset:31744
	s_waitcnt lgkmcnt(3)
	v_pk_fma_f32 v[162:163], v[92:93], v[236:237], v[162:163] op_sel_hi:[1,0,1]
	s_nop 0
	v_pk_fma_f32 v[158:159], v[94:95], v[236:237], v[162:163] op_sel:[0,1,0]
	s_nop 0
	v_pk_fma_f32 v[158:159], v[100:101], v[238:239], v[158:159] op_sel_hi:[1,0,1]
	v_mov_b32_e32 v160, v239
	v_pk_fma_f32 v[162:163], v[104:105], v[160:161], v[158:159] op_sel_hi:[1,0,1]
	ds_read_b128 v[232:235], v182 offset:32768
	s_waitcnt lgkmcnt(3)
	v_pk_fma_f32 v[162:163], v[80:81], v[240:241], v[162:163] op_sel_hi:[1,0,1]
	s_nop 0
	v_pk_fma_f32 v[158:159], v[82:83], v[240:241], v[162:163] op_sel:[0,1,0]
	s_nop 0
	v_pk_fma_f32 v[158:159], v[86:87], v[242:243], v[158:159] op_sel_hi:[1,0,1]
	v_mov_b32_e32 v160, v243
	v_pk_fma_f32 v[162:163], v[90:91], v[160:161], v[158:159] op_sel_hi:[1,0,1]
	ds_read_b128 v[236:239], v182 offset:33792
	s_waitcnt lgkmcnt(3)
	v_pk_fma_f32 v[162:163], v[76:77], v[224:225], v[162:163] op_sel_hi:[1,0,1]
	s_nop 0
	v_pk_fma_f32 v[158:159], v[78:79], v[224:225], v[162:163] op_sel:[0,1,0]
	s_nop 0
	v_pk_fma_f32 v[158:159], v[84:85], v[226:227], v[158:159] op_sel_hi:[1,0,1]
	v_mov_b32_e32 v160, v227
	v_pk_fma_f32 v[162:163], v[88:89], v[160:161], v[158:159] op_sel_hi:[1,0,1]
	ds_read_b128 v[240:243], v182 offset:34816
	s_waitcnt lgkmcnt(3)
	v_pk_fma_f32 v[162:163], v[68:69], v[228:229], v[162:163] op_sel_hi:[1,0,1]
	s_nop 0
	v_pk_fma_f32 v[158:159], v[70:71], v[228:229], v[162:163] op_sel:[0,1,0]
	s_nop 0
	v_pk_fma_f32 v[158:159], v[72:73], v[230:231], v[158:159] op_sel_hi:[1,0,1]
	v_mov_b32_e32 v160, v231
	v_pk_fma_f32 v[158:159], v[74:75], v[160:161], v[158:159] op_sel_hi:[1,0,1]
	ds_read_b128 v[224:227], v182 offset:35840
	s_waitcnt lgkmcnt(3)
	v_pk_fma_f32 v[164:165], v[124:125], v[232:233], 0 op_sel_hi:[1,0,0]
	s_nop 0
	v_pk_fma_f32 v[160:161], v[126:127], v[232:233], v[164:165] op_sel:[0,1,0]
	s_nop 0
	v_pk_fma_f32 v[160:161], v[128:129], v[234:235], v[160:161] op_sel_hi:[1,0,1]
	v_mov_b32_e32 v162, v235
	v_pk_fma_f32 v[164:165], v[130:131], v[162:163], v[160:161] op_sel_hi:[1,0,1]
	ds_read_b128 v[228:231], v182 offset:36864
	s_waitcnt lgkmcnt(3)
	v_pk_fma_f32 v[164:165], v[112:113], v[236:237], v[164:165] op_sel_hi:[1,0,1]
	s_nop 0
	v_pk_fma_f32 v[160:161], v[114:115], v[236:237], v[164:165] op_sel:[0,1,0]
	s_nop 0
	v_pk_fma_f32 v[160:161], v[118:119], v[238:239], v[160:161] op_sel_hi:[1,0,1]
	v_mov_b32_e32 v162, v239
	v_pk_fma_f32 v[164:165], v[122:123], v[162:163], v[160:161] op_sel_hi:[1,0,1]
	ds_read_b128 v[232:235], v182 offset:37888
	s_waitcnt lgkmcnt(3)
	v_pk_fma_f32 v[164:165], v[108:109], v[240:241], v[164:165] op_sel_hi:[1,0,1]
	s_nop 0
	v_pk_fma_f32 v[160:161], v[110:111], v[240:241], v[164:165] op_sel:[0,1,0]
	s_nop 0
	v_pk_fma_f32 v[160:161], v[116:117], v[242:243], v[160:161] op_sel_hi:[1,0,1]
	v_mov_b32_e32 v162, v243
	v_pk_fma_f32 v[164:165], v[120:121], v[162:163], v[160:161] op_sel_hi:[1,0,1]
	ds_read_b128 v[236:239], v182 offset:38912
	s_waitcnt lgkmcnt(3)
	v_pk_fma_f32 v[164:165], v[96:97], v[224:225], v[164:165] op_sel_hi:[1,0,1]
	s_nop 0
	v_pk_fma_f32 v[160:161], v[98:99], v[224:225], v[164:165] op_sel:[0,1,0]
	s_nop 0
	v_pk_fma_f32 v[160:161], v[102:103], v[226:227], v[160:161] op_sel_hi:[1,0,1]
	v_mov_b32_e32 v162, v227
	v_pk_fma_f32 v[164:165], v[106:107], v[162:163], v[160:161] op_sel_hi:[1,0,1]
	ds_read_b128 v[240:243], v182 offset:39936
	s_waitcnt lgkmcnt(3)
	v_pk_fma_f32 v[164:165], v[92:93], v[228:229], v[164:165] op_sel_hi:[1,0,1]
	s_nop 0
	v_pk_fma_f32 v[160:161], v[94:95], v[228:229], v[164:165] op_sel:[0,1,0]
	s_nop 0
	v_pk_fma_f32 v[160:161], v[100:101], v[230:231], v[160:161] op_sel_hi:[1,0,1]
	v_mov_b32_e32 v162, v231
	v_pk_fma_f32 v[164:165], v[104:105], v[162:163], v[160:161] op_sel_hi:[1,0,1]
	ds_read_b128 v[224:227], v182 offset:40960
	s_waitcnt lgkmcnt(3)
	v_pk_fma_f32 v[164:165], v[80:81], v[232:233], v[164:165] op_sel_hi:[1,0,1]
	s_nop 0
	v_pk_fma_f32 v[160:161], v[82:83], v[232:233], v[164:165] op_sel:[0,1,0]
	s_nop 0
	v_pk_fma_f32 v[160:161], v[86:87], v[234:235], v[160:161] op_sel_hi:[1,0,1]
	v_mov_b32_e32 v162, v235
	v_pk_fma_f32 v[164:165], v[90:91], v[162:163], v[160:161] op_sel_hi:[1,0,1]
	ds_read_b128 v[228:231], v182 offset:41984
	s_waitcnt lgkmcnt(3)
	v_pk_fma_f32 v[164:165], v[76:77], v[236:237], v[164:165] op_sel_hi:[1,0,1]
	s_nop 0
	v_pk_fma_f32 v[160:161], v[78:79], v[236:237], v[164:165] op_sel:[0,1,0]
	s_nop 0
	v_pk_fma_f32 v[160:161], v[84:85], v[238:239], v[160:161] op_sel_hi:[1,0,1]
	v_mov_b32_e32 v162, v239
	v_pk_fma_f32 v[164:165], v[88:89], v[162:163], v[160:161] op_sel_hi:[1,0,1]
	ds_read_b128 v[232:235], v182 offset:43008
	s_waitcnt lgkmcnt(3)
	v_pk_fma_f32 v[164:165], v[68:69], v[240:241], v[164:165] op_sel_hi:[1,0,1]
	s_nop 0
	v_pk_fma_f32 v[160:161], v[70:71], v[240:241], v[164:165] op_sel:[0,1,0]
	s_nop 0
	v_pk_fma_f32 v[160:161], v[72:73], v[242:243], v[160:161] op_sel_hi:[1,0,1]
	v_mov_b32_e32 v162, v243
	v_pk_fma_f32 v[160:161], v[74:75], v[162:163], v[160:161] op_sel_hi:[1,0,1]
	ds_read_b128 v[236:239], v182 offset:44032
	s_waitcnt lgkmcnt(3)
	v_pk_fma_f32 v[166:167], v[124:125], v[224:225], 0 op_sel_hi:[1,0,0]
	s_nop 0
	v_pk_fma_f32 v[162:163], v[126:127], v[224:225], v[166:167] op_sel:[0,1,0]
	s_nop 0
	v_pk_fma_f32 v[162:163], v[128:129], v[226:227], v[162:163] op_sel_hi:[1,0,1]
	v_mov_b32_e32 v164, v227
	v_pk_fma_f32 v[166:167], v[130:131], v[164:165], v[162:163] op_sel_hi:[1,0,1]
	ds_read_b128 v[240:243], v182 offset:45056
	s_waitcnt lgkmcnt(3)
; #define LAS __attribute__((address_space(3)))
; __device__ __forceinline__ float bflo(unsigned w) { return __uint_as_float(w << 16); }
; __device__ __forceinline__ float bfhi(unsigned w) { return __uint_as_float(w & 0xffff0000u); }
; __device__ __forceinline__ void phase_norm2(const Params& p, const Ctx& F, const int l) {
;     ...
;         { const float* xlat = l == 0 ? p.x : p.out; const float* xctx = l == 0 ? p.ctx : F.xc;
;           const float* xs0 = isctx ? xctx + ((size_t)b * CTXL + t) * DM : xlat + ((size_t)b * SEQ + (t - CTXL)) * DM;
;           const float* xs1 = two ? xlat + ((size_t)b * SEQ + (tB - CTXL)) * DM : xs0;
;           const bf16_t* d0p = F.dlt + ((size_t)b * TPB + t) * DM + 4 * F.lane; const bf16_t* d1p = F.dlt + ((size_t)b * TPB + (two ? tB : t)) * DM + 4 * F.lane;
; #pragma unroll
;           for (int j = 0; j < 8; ++j) { f32x4 x0 = __builtin_nontemporal_load((const f32x4*)xs0 + F.lane + 64 * j), x1 = __builtin_nontemporal_load((const f32x4*)xs1 + F.lane + 64 * j);
;               const u32x2 e0 = __builtin_nontemporal_load((const u32x2*)(d0p + 256 * j)), e1 = __builtin_nontemporal_load((const u32x2*)(d1p + 256 * j));
;               x0 += (f32x4){bflo(e0.x), bfhi(e0.x), bflo(e0.y), bfhi(e0.y)}; x1 += (f32x4){bflo(e1.x), bfhi(e1.x), bflo(e1.y), bfhi(e1.y)};
; #pragma unroll
;               for (int c = 0; c < 4; ++c) vv[j][c] = (f32x2){x0[c], x1[c]}; } }
;     ...
; #pragma unroll
;         for (int e = 0; e < 16; ++e) { f32x2 a = {0.f, 0.f};
; #pragma unroll
;             for (int j = 0; j < 8; ++j) { const f32x4 w = *((const LAS f32x4*)(wr2 + e * DM) + F.lane + 64 * j);
; #pragma unroll
;                 for (int c = 0; c < 4; ++c) a += vv[j][c] * w[c]; }
;             lg[e] = a; }
	v_pk_fma_f32 v[166:167], v[112:113], v[228:229], v[166:167] op_sel_hi:[1,0,1]
	s_nop 0
	v_pk_fma_f32 v[162:163], v[114:115], v[228:229], v[166:167] op_sel:[0,1,0]
	s_nop 0
	v_pk_fma_f32 v[162:163], v[118:119], v[230:231], v[162:163] op_sel_hi:[1,0,1]
	v_mov_b32_e32 v164, v231
	v_pk_fma_f32 v[166:167], v[122:123], v[164:165], v[162:163] op_sel_hi:[1,0,1]
	ds_read_b128 v[224:227], v182 offset:46080
	s_waitcnt lgkmcnt(3)
	v_pk_fma_f32 v[166:167], v[108:109], v[232:233], v[166:167] op_sel_hi:[1,0,1]
	s_nop 0
	v_pk_fma_f32 v[162:163], v[110:111], v[232:233], v[166:167] op_sel:[0,1,0]
	s_nop 0
	v_pk_fma_f32 v[162:163], v[116:117], v[234:235], v[162:163] op_sel_hi:[1,0,1]
	v_mov_b32_e32 v164, v235
	v_pk_fma_f32 v[166:167], v[120:121], v[164:165], v[162:163] op_sel_hi:[1,0,1]
	ds_read_b128 v[228:231], v182 offset:47104
	s_waitcnt lgkmcnt(3)
	v_pk_fma_f32 v[166:167], v[96:97], v[236:237], v[166:167] op_sel_hi:[1,0,1]
	s_nop 0
	v_pk_fma_f32 v[162:163], v[98:99], v[236:237], v[166:167] op_sel:[0,1,0]
	s_nop 0
	v_pk_fma_f32 v[162:163], v[102:103], v[238:239], v[162:163] op_sel_hi:[1,0,1]
	v_mov_b32_e32 v164, v239
	v_pk_fma_f32 v[166:167], v[106:107], v[164:165], v[162:163] op_sel_hi:[1,0,1]
	ds_read_b128 v[232:235], v182 offset:48128
	s_waitcnt lgkmcnt(3)
	v_pk_fma_f32 v[166:167], v[92:93], v[240:241], v[166:167] op_sel_hi:[1,0,1]
	s_nop 0
	v_pk_fma_f32 v[162:163], v[94:95], v[240:241], v[166:167] op_sel:[0,1,0]
	s_nop 0
	v_pk_fma_f32 v[162:163], v[100:101], v[242:243], v[162:163] op_sel_hi:[1,0,1]
	v_mov_b32_e32 v164, v243
	v_pk_fma_f32 v[166:167], v[104:105], v[164:165], v[162:163] op_sel_hi:[1,0,1]
	ds_read_b128 v[236:239], v182 offset:49152
	s_waitcnt lgkmcnt(3)
	v_pk_fma_f32 v[166:167], v[80:81], v[224:225], v[166:167] op_sel_hi:[1,0,1]
	s_nop 0
	v_pk_fma_f32 v[162:163], v[82:83], v[224:225], v[166:167] op_sel:[0,1,0]
	s_nop 0
	v_pk_fma_f32 v[162:163], v[86:87], v[226:227], v[162:163] op_sel_hi:[1,0,1]
	v_mov_b32_e32 v164, v227
	v_pk_fma_f32 v[166:167], v[90:91], v[164:165], v[162:163] op_sel_hi:[1,0,1]
	ds_read_b128 v[240:243], v182 offset:50176
	s_waitcnt lgkmcnt(3)
	v_pk_fma_f32 v[166:167], v[76:77], v[228:229], v[166:167] op_sel_hi:[1,0,1]
	s_nop 0
	v_pk_fma_f32 v[162:163], v[78:79], v[228:229], v[166:167] op_sel:[0,1,0]
	s_nop 0
	v_pk_fma_f32 v[162:163], v[84:85], v[230:231], v[162:163] op_sel_hi:[1,0,1]
	v_mov_b32_e32 v164, v231
	v_pk_fma_f32 v[166:167], v[88:89], v[164:165], v[162:163] op_sel_hi:[1,0,1]
	ds_read_b128 v[224:227], v182 offset:51200
	s_waitcnt lgkmcnt(3)
	v_pk_fma_f32 v[166:167], v[68:69], v[232:233], v[166:167] op_sel_hi:[1,0,1]
	s_nop 0
	v_pk_fma_f32 v[162:163], v[70:71], v[232:233], v[166:167] op_sel:[0,1,0]
	s_nop 0
	v_pk_fma_f32 v[162:163], v[72:73], v[234:235], v[162:163] op_sel_hi:[1,0,1]
	v_mov_b32_e32 v164, v235
	v_pk_fma_f32 v[162:163], v[74:75], v[164:165], v[162:163] op_sel_hi:[1,0,1]
	s_cmpk_gt_i32 s60, 0xff
	s_cbranch_scc0 .Lpf_done
	s_add_i32 s59, s60, s16
	s_cmpk_lt_i32 s59, 0x1100
	s_cbranch_scc0 .Lpf_done
	s_add_i32 s58, s59, s16
	s_cmpk_lt_i32 s58, 0x1100
	s_cbranch_scc0 .Lpf_done
	v_lshlrev_b32_e32 v202, 4, v132
	s_add_i32 s94, s58, s25
	s_addk_i32 s94, 0xff00
	s_mov_b32 s95, 0
	s_lshl_b64 s[94:95], s[94:95], 13
	s_add_u32 s94, s19, s94
	s_addc_u32 s95, s18, s95
	global_load_dwordx4 v[204:207], v202, s[94:95]
	global_load_dwordx4 v[204:207], v202, s[94:95] offset:1024
	global_load_dwordx4 v[204:207], v202, s[94:95] offset:2048
	global_load_dwordx4 v[204:207], v202, s[94:95] offset:3072
	s_add_u32 s94, s94, 0x1000
	s_addc_u32 s95, s95, 0
	global_load_dwordx4 v[204:207], v202, s[94:95]
	global_load_dwordx4 v[204:207], v202, s[94:95] offset:1024
	global_load_dwordx4 v[204:207], v202, s[94:95] offset:2048
	global_load_dwordx4 v[204:207], v202, s[94:95] offset:3072
	s_add_i32 s96, s58, s26
	s_mov_b32 s97, 0
	s_lshl_b64 s[96:97], s[96:97], 12
	v_lshl_add_u64 v[210:211], v[134:135], 0, s[96:97]
	global_load_dwordx2 v[208:209], v[210:211], off
	global_load_dwordx2 v[208:209], v[210:211], off offset:512
	global_load_dwordx2 v[208:209], v[210:211], off offset:1024
	global_load_dwordx2 v[208:209], v[210:211], off offset:1536
	global_load_dwordx2 v[208:209], v[210:211], off offset:2048
	global_load_dwordx2 v[208:209], v[210:211], off offset:2560
	global_load_dwordx2 v[208:209], v[210:211], off offset:3072
	global_load_dwordx2 v[208:209], v[210:211], off offset:3584
	s_add_i32 s58, s58, s16
	s_cmpk_lt_i32 s58, 0x1100
	s_cbranch_scc0 .Lpf_done
	s_add_i32 s94, s58, s25
	s_addk_i32 s94, 0xff00
	s_mov_b32 s95, 0
	s_lshl_b64 s[94:95], s[94:95], 13
	s_add_u32 s94, s19, s94
	s_addc_u32 s95, s18, s95
	global_load_dwordx4 v[204:207], v202, s[94:95]
	global_load_dwordx4 v[204:207], v202, s[94:95] offset:1024
	global_load_dwordx4 v[204:207], v202, s[94:95] offset:2048
	global_load_dwordx4 v[204:207], v202, s[94:95] offset:3072
	s_add_u32 s94, s94, 0x1000
	s_addc_u32 s95, s95, 0
	global_load_dwordx4 v[204:207], v202, s[94:95]
	global_load_dwordx4 v[204:207], v202, s[94:95] offset:1024
	global_load_dwordx4 v[204:207], v202, s[94:95] offset:2048
	global_load_dwordx4 v[204:207], v202, s[94:95] offset:3072
	s_add_i32 s96, s58, s26
	s_mov_b32 s97, 0
	s_lshl_b64 s[96:97], s[96:97], 12
	v_lshl_add_u64 v[210:211], v[134:135], 0, s[96:97]
	global_load_dwordx2 v[208:209], v[210:211], off
	global_load_dwordx2 v[208:209], v[210:211], off offset:512
	global_load_dwordx2 v[208:209], v[210:211], off offset:1024
	global_load_dwordx2 v[208:209], v[210:211], off offset:1536
	global_load_dwordx2 v[208:209], v[210:211], off offset:2048
	global_load_dwordx2 v[208:209], v[210:211], off offset:2560
	global_load_dwordx2 v[208:209], v[210:211], off offset:3072
	global_load_dwordx2 v[208:209], v[210:211], off offset:3584
; #define LAS __attribute__((address_space(3)))
; __device__ __forceinline__ void phase_norm2(const Params& p, const Ctx& F, const int l) {
;     ...
; #pragma unroll
;         for (int e = 0; e < 16; ++e) { f32x2 a = {0.f, 0.f};
; #pragma unroll
;             for (int j = 0; j < 8; ++j) { const f32x4 w = *((const LAS f32x4*)(wr2 + e * DM) + F.lane + 64 * j);
; #pragma unroll
;                 for (int c = 0; c < 4; ++c) a += vv[j][c] * w[c]; }
;             lg[e] = a; }
.Lpf_done:
	ds_read_b128 v[228:231], v182 offset:52224
	s_waitcnt lgkmcnt(3)
	v_pk_fma_f32 v[168:169], v[124:125], v[236:237], 0 op_sel_hi:[1,0,0]
	s_nop 0
	v_pk_fma_f32 v[164:165], v[126:127], v[236:237], v[168:169] op_sel:[0,1,0]
	s_nop 0
	v_pk_fma_f32 v[164:165], v[128:129], v[238:239], v[164:165] op_sel_hi:[1,0,1]
	v_mov_b32_e32 v166, v239
	v_pk_fma_f32 v[168:169], v[130:131], v[166:167], v[164:165] op_sel_hi:[1,0,1]
	ds_read_b128 v[232:235], v182 offset:53248
	s_waitcnt lgkmcnt(3)
	v_pk_fma_f32 v[168:169], v[112:113], v[240:241], v[168:169] op_sel_hi:[1,0,1]
	s_nop 0
	v_pk_fma_f32 v[164:165], v[114:115], v[240:241], v[168:169] op_sel:[0,1,0]
	s_nop 0
	v_pk_fma_f32 v[164:165], v[118:119], v[242:243], v[164:165] op_sel_hi:[1,0,1]
	v_mov_b32_e32 v166, v243
	v_pk_fma_f32 v[168:169], v[122:123], v[166:167], v[164:165] op_sel_hi:[1,0,1]
	ds_read_b128 v[236:239], v182 offset:54272
	s_waitcnt lgkmcnt(3)
	v_pk_fma_f32 v[168:169], v[108:109], v[224:225], v[168:169] op_sel_hi:[1,0,1]
	s_nop 0
	v_pk_fma_f32 v[164:165], v[110:111], v[224:225], v[168:169] op_sel:[0,1,0]
	s_nop 0
	v_pk_fma_f32 v[164:165], v[116:117], v[226:227], v[164:165] op_sel_hi:[1,0,1]
	v_mov_b32_e32 v166, v227
	v_pk_fma_f32 v[168:169], v[120:121], v[166:167], v[164:165] op_sel_hi:[1,0,1]
	ds_read_b128 v[240:243], v182 offset:55296
	s_waitcnt lgkmcnt(3)
	v_pk_fma_f32 v[168:169], v[96:97], v[228:229], v[168:169] op_sel_hi:[1,0,1]
	s_nop 0
	v_pk_fma_f32 v[164:165], v[98:99], v[228:229], v[168:169] op_sel:[0,1,0]
	s_nop 0
	v_pk_fma_f32 v[164:165], v[102:103], v[230:231], v[164:165] op_sel_hi:[1,0,1]
	v_mov_b32_e32 v166, v231
	v_pk_fma_f32 v[168:169], v[106:107], v[166:167], v[164:165] op_sel_hi:[1,0,1]
	ds_read_b128 v[224:227], v182 offset:56320
	s_waitcnt lgkmcnt(3)
	v_pk_fma_f32 v[168:169], v[92:93], v[232:233], v[168:169] op_sel_hi:[1,0,1]
	s_nop 0
	v_pk_fma_f32 v[164:165], v[94:95], v[232:233], v[168:169] op_sel:[0,1,0]
	s_nop 0
	v_pk_fma_f32 v[164:165], v[100:101], v[234:235], v[164:165] op_sel_hi:[1,0,1]
	v_mov_b32_e32 v166, v235
	v_pk_fma_f32 v[168:169], v[104:105], v[166:167], v[164:165] op_sel_hi:[1,0,1]
	ds_read_b128 v[228:231], v182 offset:57344
	s_waitcnt lgkmcnt(3)
	v_pk_fma_f32 v[168:169], v[80:81], v[236:237], v[168:169] op_sel_hi:[1,0,1]
	s_nop 0
	v_pk_fma_f32 v[164:165], v[82:83], v[236:237], v[168:169] op_sel:[0,1,0]
	s_nop 0
	v_pk_fma_f32 v[164:165], v[86:87], v[238:239], v[164:165] op_sel_hi:[1,0,1]
	v_mov_b32_e32 v166, v239
	v_pk_fma_f32 v[168:169], v[90:91], v[166:167], v[164:165] op_sel_hi:[1,0,1]
	ds_read_b128 v[232:235], v182 offset:58368
	s_waitcnt lgkmcnt(3)
	v_pk_fma_f32 v[168:169], v[76:77], v[240:241], v[168:169] op_sel_hi:[1,0,1]
	s_nop 0
	v_pk_fma_f32 v[164:165], v[78:79], v[240:241], v[168:169] op_sel:[0,1,0]
	s_nop 0
	v_pk_fma_f32 v[164:165], v[84:85], v[242:243], v[164:165] op_sel_hi:[1,0,1]
	v_mov_b32_e32 v166, v243
	v_pk_fma_f32 v[168:169], v[88:89], v[166:167], v[164:165] op_sel_hi:[1,0,1]
	ds_read_b128 v[236:239], v182 offset:59392
	s_waitcnt lgkmcnt(3)
	v_pk_fma_f32 v[168:169], v[68:69], v[224:225], v[168:169] op_sel_hi:[1,0,1]
	s_nop 0
	v_pk_fma_f32 v[164:165], v[70:71], v[224:225], v[168:169] op_sel:[0,1,0]
	s_nop 0
	v_pk_fma_f32 v[164:165], v[72:73], v[226:227], v[164:165] op_sel_hi:[1,0,1]
	v_mov_b32_e32 v166, v227
	v_pk_fma_f32 v[164:165], v[74:75], v[166:167], v[164:165] op_sel_hi:[1,0,1]
	ds_read_b128 v[240:243], v182 offset:60416
	s_waitcnt lgkmcnt(3)
	v_pk_fma_f32 v[170:171], v[124:125], v[228:229], 0 op_sel_hi:[1,0,0]
	s_nop 0
	v_pk_fma_f32 v[166:167], v[126:127], v[228:229], v[170:171] op_sel:[0,1,0]
	s_nop 0
	v_pk_fma_f32 v[166:167], v[128:129], v[230:231], v[166:167] op_sel_hi:[1,0,1]
	v_mov_b32_e32 v168, v231
	v_pk_fma_f32 v[170:171], v[130:131], v[168:169], v[166:167] op_sel_hi:[1,0,1]
	ds_read_b128 v[224:227], v182 offset:61440
	s_waitcnt lgkmcnt(3)
	v_pk_fma_f32 v[170:171], v[112:113], v[232:233], v[170:171] op_sel_hi:[1,0,1]
	s_nop 0
	v_pk_fma_f32 v[166:167], v[114:115], v[232:233], v[170:171] op_sel:[0,1,0]
	s_nop 0
	v_pk_fma_f32 v[166:167], v[118:119], v[234:235], v[166:167] op_sel_hi:[1,0,1]
	v_mov_b32_e32 v168, v235
	v_pk_fma_f32 v[170:171], v[122:123], v[168:169], v[166:167] op_sel_hi:[1,0,1]
	ds_read_b128 v[228:231], v182 offset:62464
	s_waitcnt lgkmcnt(3)
	v_pk_fma_f32 v[170:171], v[108:109], v[236:237], v[170:171] op_sel_hi:[1,0,1]
	s_nop 0
	v_pk_fma_f32 v[166:167], v[110:111], v[236:237], v[170:171] op_sel:[0,1,0]
	s_nop 0
	v_pk_fma_f32 v[166:167], v[116:117], v[238:239], v[166:167] op_sel_hi:[1,0,1]
	v_mov_b32_e32 v168, v239
	v_pk_fma_f32 v[170:171], v[120:121], v[168:169], v[166:167] op_sel_hi:[1,0,1]
	ds_read_b128 v[232:235], v182 offset:63488
	s_waitcnt lgkmcnt(3)
	v_pk_fma_f32 v[170:171], v[96:97], v[240:241], v[170:171] op_sel_hi:[1,0,1]
	s_nop 0
	v_pk_fma_f32 v[166:167], v[98:99], v[240:241], v[170:171] op_sel:[0,1,0]
	s_nop 0
	v_pk_fma_f32 v[166:167], v[102:103], v[242:243], v[166:167] op_sel_hi:[1,0,1]
	v_mov_b32_e32 v168, v243
	v_pk_fma_f32 v[170:171], v[106:107], v[168:169], v[166:167] op_sel_hi:[1,0,1]
	ds_read_b128 v[236:239], v182 offset:64512
	s_waitcnt lgkmcnt(3)
	v_pk_fma_f32 v[170:171], v[92:93], v[224:225], v[170:171] op_sel_hi:[1,0,1]
	s_nop 0
	v_pk_fma_f32 v[166:167], v[94:95], v[224:225], v[170:171] op_sel:[0,1,0]
	s_nop 0
	v_pk_fma_f32 v[166:167], v[100:101], v[226:227], v[166:167] op_sel_hi:[1,0,1]
	v_mov_b32_e32 v168, v227
	v_pk_fma_f32 v[170:171], v[104:105], v[168:169], v[166:167] op_sel_hi:[1,0,1]
	ds_read_b128 v[240:243], v244
	s_waitcnt lgkmcnt(3)
; #define LAS __attribute__((address_space(3)))
; __device__ __forceinline__ void phase_norm2(const Params& p, const Ctx& F, const int l) {
;     ...
; #pragma unroll
;         for (int e = 0; e < 16; ++e) { f32x2 a = {0.f, 0.f};
; #pragma unroll
;             for (int j = 0; j < 8; ++j) { const f32x4 w = *((const LAS f32x4*)(wr2 + e * DM) + F.lane + 64 * j);
; #pragma unroll
;                 for (int c = 0; c < 4; ++c) a += vv[j][c] * w[c]; }
;             lg[e] = a; }
	v_pk_fma_f32 v[170:171], v[80:81], v[228:229], v[170:171] op_sel_hi:[1,0,1]
	s_nop 0
	v_pk_fma_f32 v[166:167], v[82:83], v[228:229], v[170:171] op_sel:[0,1,0]
	s_nop 0
	v_pk_fma_f32 v[166:167], v[86:87], v[230:231], v[166:167] op_sel_hi:[1,0,1]
	v_mov_b32_e32 v168, v231
	v_pk_fma_f32 v[170:171], v[90:91], v[168:169], v[166:167] op_sel_hi:[1,0,1]
	ds_read_b128 v[224:227], v244 offset:1024
	s_waitcnt lgkmcnt(3)
	v_pk_fma_f32 v[170:171], v[76:77], v[232:233], v[170:171] op_sel_hi:[1,0,1]
	s_nop 0
	v_pk_fma_f32 v[166:167], v[78:79], v[232:233], v[170:171] op_sel:[0,1,0]
	s_nop 0
	v_pk_fma_f32 v[166:167], v[84:85], v[234:235], v[166:167] op_sel_hi:[1,0,1]
	v_mov_b32_e32 v168, v235
	v_pk_fma_f32 v[170:171], v[88:89], v[168:169], v[166:167] op_sel_hi:[1,0,1]
	ds_read_b128 v[228:231], v244 offset:2048
	s_waitcnt lgkmcnt(3)
	v_pk_fma_f32 v[170:171], v[68:69], v[236:237], v[170:171] op_sel_hi:[1,0,1]
	s_nop 0
	v_pk_fma_f32 v[166:167], v[70:71], v[236:237], v[170:171] op_sel:[0,1,0]
	s_nop 0
	v_pk_fma_f32 v[166:167], v[72:73], v[238:239], v[166:167] op_sel_hi:[1,0,1]
	v_mov_b32_e32 v168, v239
	v_pk_fma_f32 v[166:167], v[74:75], v[168:169], v[166:167] op_sel_hi:[1,0,1]
	ds_read_b128 v[232:235], v244 offset:3072
	s_waitcnt lgkmcnt(3)
	v_pk_fma_f32 v[172:173], v[124:125], v[240:241], 0 op_sel_hi:[1,0,0]
	s_nop 0
	v_pk_fma_f32 v[168:169], v[126:127], v[240:241], v[172:173] op_sel:[0,1,0]
	s_nop 0
	v_pk_fma_f32 v[168:169], v[128:129], v[242:243], v[168:169] op_sel_hi:[1,0,1]
	v_mov_b32_e32 v170, v243
	v_pk_fma_f32 v[172:173], v[130:131], v[170:171], v[168:169] op_sel_hi:[1,0,1]
	ds_read_b128 v[236:239], v244 offset:4096
	s_waitcnt lgkmcnt(3)
	v_pk_fma_f32 v[172:173], v[112:113], v[224:225], v[172:173] op_sel_hi:[1,0,1]
	s_nop 0
	v_pk_fma_f32 v[168:169], v[114:115], v[224:225], v[172:173] op_sel:[0,1,0]
	s_nop 0
	v_pk_fma_f32 v[168:169], v[118:119], v[226:227], v[168:169] op_sel_hi:[1,0,1]
	v_mov_b32_e32 v170, v227
	v_pk_fma_f32 v[172:173], v[122:123], v[170:171], v[168:169] op_sel_hi:[1,0,1]
	ds_read_b128 v[240:243], v244 offset:5120
	s_waitcnt lgkmcnt(3)
	v_pk_fma_f32 v[172:173], v[108:109], v[228:229], v[172:173] op_sel_hi:[1,0,1]
	s_nop 0
	v_pk_fma_f32 v[168:169], v[110:111], v[228:229], v[172:173] op_sel:[0,1,0]
	s_nop 0
	v_pk_fma_f32 v[168:169], v[116:117], v[230:231], v[168:169] op_sel_hi:[1,0,1]
	v_mov_b32_e32 v170, v231
	v_pk_fma_f32 v[172:173], v[120:121], v[170:171], v[168:169] op_sel_hi:[1,0,1]
	ds_read_b128 v[224:227], v244 offset:6144
	s_waitcnt lgkmcnt(3)
	v_pk_fma_f32 v[172:173], v[96:97], v[232:233], v[172:173] op_sel_hi:[1,0,1]
	s_nop 0
	v_pk_fma_f32 v[168:169], v[98:99], v[232:233], v[172:173] op_sel:[0,1,0]
	s_nop 0
	v_pk_fma_f32 v[168:169], v[102:103], v[234:235], v[168:169] op_sel_hi:[1,0,1]
	v_mov_b32_e32 v170, v235
	v_pk_fma_f32 v[172:173], v[106:107], v[170:171], v[168:169] op_sel_hi:[1,0,1]
	ds_read_b128 v[228:231], v244 offset:7168
	s_waitcnt lgkmcnt(3)
	v_pk_fma_f32 v[172:173], v[92:93], v[236:237], v[172:173] op_sel_hi:[1,0,1]
	s_nop 0
	v_pk_fma_f32 v[168:169], v[94:95], v[236:237], v[172:173] op_sel:[0,1,0]
	s_nop 0
	v_pk_fma_f32 v[168:169], v[100:101], v[238:239], v[168:169] op_sel_hi:[1,0,1]
	v_mov_b32_e32 v170, v239
	v_pk_fma_f32 v[172:173], v[104:105], v[170:171], v[168:169] op_sel_hi:[1,0,1]
	ds_read_b128 v[232:235], v244 offset:8192
	s_waitcnt lgkmcnt(3)
	v_pk_fma_f32 v[172:173], v[80:81], v[240:241], v[172:173] op_sel_hi:[1,0,1]
	s_nop 0
	v_pk_fma_f32 v[168:169], v[82:83], v[240:241], v[172:173] op_sel:[0,1,0]
	s_nop 0
	v_pk_fma_f32 v[168:169], v[86:87], v[242:243], v[168:169] op_sel_hi:[1,0,1]
	v_mov_b32_e32 v170, v243
	v_pk_fma_f32 v[172:173], v[90:91], v[170:171], v[168:169] op_sel_hi:[1,0,1]
	ds_read_b128 v[236:239], v244 offset:9216
	s_waitcnt lgkmcnt(3)
	v_pk_fma_f32 v[172:173], v[76:77], v[224:225], v[172:173] op_sel_hi:[1,0,1]
	s_nop 0
	v_pk_fma_f32 v[168:169], v[78:79], v[224:225], v[172:173] op_sel:[0,1,0]
	s_nop 0
	v_pk_fma_f32 v[168:169], v[84:85], v[226:227], v[168:169] op_sel_hi:[1,0,1]
	v_mov_b32_e32 v170, v227
	v_pk_fma_f32 v[172:173], v[88:89], v[170:171], v[168:169] op_sel_hi:[1,0,1]
	ds_read_b128 v[240:243], v244 offset:10240
	s_waitcnt lgkmcnt(3)
	v_pk_fma_f32 v[172:173], v[68:69], v[228:229], v[172:173] op_sel_hi:[1,0,1]
	s_nop 0
	v_pk_fma_f32 v[168:169], v[70:71], v[228:229], v[172:173] op_sel:[0,1,0]
	s_nop 0
	v_pk_fma_f32 v[168:169], v[72:73], v[230:231], v[168:169] op_sel_hi:[1,0,1]
	v_mov_b32_e32 v170, v231
	v_pk_fma_f32 v[168:169], v[74:75], v[170:171], v[168:169] op_sel_hi:[1,0,1]
	ds_read_b128 v[224:227], v244 offset:11264
	s_waitcnt lgkmcnt(3)
	v_pk_fma_f32 v[174:175], v[124:125], v[232:233], 0 op_sel_hi:[1,0,0]
	s_nop 0
	v_pk_fma_f32 v[170:171], v[126:127], v[232:233], v[174:175] op_sel:[0,1,0]
	s_nop 0
	v_pk_fma_f32 v[170:171], v[128:129], v[234:235], v[170:171] op_sel_hi:[1,0,1]
	v_mov_b32_e32 v172, v235
	v_pk_fma_f32 v[174:175], v[130:131], v[172:173], v[170:171] op_sel_hi:[1,0,1]
	ds_read_b128 v[228:231], v244 offset:12288
	s_waitcnt lgkmcnt(3)
	v_pk_fma_f32 v[174:175], v[112:113], v[236:237], v[174:175] op_sel_hi:[1,0,1]
	s_nop 0
	v_pk_fma_f32 v[170:171], v[114:115], v[236:237], v[174:175] op_sel:[0,1,0]
	s_nop 0
	v_pk_fma_f32 v[170:171], v[118:119], v[238:239], v[170:171] op_sel_hi:[1,0,1]
	v_mov_b32_e32 v172, v239
	v_pk_fma_f32 v[174:175], v[122:123], v[172:173], v[170:171] op_sel_hi:[1,0,1]
	ds_read_b128 v[232:235], v244 offset:13312
	s_waitcnt lgkmcnt(3)
	v_pk_fma_f32 v[174:175], v[108:109], v[240:241], v[174:175] op_sel_hi:[1,0,1]
	s_nop 0
	v_pk_fma_f32 v[170:171], v[110:111], v[240:241], v[174:175] op_sel:[0,1,0]
	s_nop 0
	v_pk_fma_f32 v[170:171], v[116:117], v[242:243], v[170:171] op_sel_hi:[1,0,1]
	v_mov_b32_e32 v172, v243
	v_pk_fma_f32 v[174:175], v[120:121], v[172:173], v[170:171] op_sel_hi:[1,0,1]
	ds_read_b128 v[236:239], v244 offset:14336
	s_waitcnt lgkmcnt(3)
; #define LAS __attribute__((address_space(3)))
; __device__ __forceinline__ void phase_norm2(const Params& p, const Ctx& F, const int l) {
;     ...
; #pragma unroll
;         for (int e = 0; e < 16; ++e) { f32x2 a = {0.f, 0.f};
; #pragma unroll
;             for (int j = 0; j < 8; ++j) { const f32x4 w = *((const LAS f32x4*)(wr2 + e * DM) + F.lane + 64 * j);
; #pragma unroll
;                 for (int c = 0; c < 4; ++c) a += vv[j][c] * w[c]; }
;             lg[e] = a; }
	v_pk_fma_f32 v[174:175], v[96:97], v[224:225], v[174:175] op_sel_hi:[1,0,1]
	s_nop 0
	v_pk_fma_f32 v[170:171], v[98:99], v[224:225], v[174:175] op_sel:[0,1,0]
	s_nop 0
	v_pk_fma_f32 v[170:171], v[102:103], v[226:227], v[170:171] op_sel_hi:[1,0,1]
	v_mov_b32_e32 v172, v227
	v_pk_fma_f32 v[174:175], v[106:107], v[172:173], v[170:171] op_sel_hi:[1,0,1]
	ds_read_b128 v[240:243], v244 offset:15360
	s_waitcnt lgkmcnt(3)
	v_pk_fma_f32 v[174:175], v[92:93], v[228:229], v[174:175] op_sel_hi:[1,0,1]
	s_nop 0
	v_pk_fma_f32 v[170:171], v[94:95], v[228:229], v[174:175] op_sel:[0,1,0]
	s_nop 0
	v_pk_fma_f32 v[170:171], v[100:101], v[230:231], v[170:171] op_sel_hi:[1,0,1]
	v_mov_b32_e32 v172, v231
	v_pk_fma_f32 v[174:175], v[104:105], v[172:173], v[170:171] op_sel_hi:[1,0,1]
	ds_read_b128 v[224:227], v244 offset:16384
	s_waitcnt lgkmcnt(3)
	v_pk_fma_f32 v[174:175], v[80:81], v[232:233], v[174:175] op_sel_hi:[1,0,1]
	s_nop 0
	v_pk_fma_f32 v[170:171], v[82:83], v[232:233], v[174:175] op_sel:[0,1,0]
	s_nop 0
	v_pk_fma_f32 v[170:171], v[86:87], v[234:235], v[170:171] op_sel_hi:[1,0,1]
	v_mov_b32_e32 v172, v235
	v_pk_fma_f32 v[174:175], v[90:91], v[172:173], v[170:171] op_sel_hi:[1,0,1]
	ds_read_b128 v[228:231], v244 offset:17408
	s_waitcnt lgkmcnt(3)
	v_pk_fma_f32 v[174:175], v[76:77], v[236:237], v[174:175] op_sel_hi:[1,0,1]
	s_nop 0
	v_pk_fma_f32 v[170:171], v[78:79], v[236:237], v[174:175] op_sel:[0,1,0]
	s_nop 0
	v_pk_fma_f32 v[170:171], v[84:85], v[238:239], v[170:171] op_sel_hi:[1,0,1]
	v_mov_b32_e32 v172, v239
	v_pk_fma_f32 v[174:175], v[88:89], v[172:173], v[170:171] op_sel_hi:[1,0,1]
	ds_read_b128 v[232:235], v244 offset:18432
	s_waitcnt lgkmcnt(3)
	v_pk_fma_f32 v[174:175], v[68:69], v[240:241], v[174:175] op_sel_hi:[1,0,1]
	s_nop 0
	v_pk_fma_f32 v[170:171], v[70:71], v[240:241], v[174:175] op_sel:[0,1,0]
	s_nop 0
	v_pk_fma_f32 v[170:171], v[72:73], v[242:243], v[170:171] op_sel_hi:[1,0,1]
	v_mov_b32_e32 v172, v243
	v_pk_fma_f32 v[170:171], v[74:75], v[172:173], v[170:171] op_sel_hi:[1,0,1]
	ds_read_b128 v[236:239], v244 offset:19456
	s_waitcnt lgkmcnt(3)
	v_pk_fma_f32 v[176:177], v[124:125], v[224:225], 0 op_sel_hi:[1,0,0]
	s_nop 0
	v_pk_fma_f32 v[172:173], v[126:127], v[224:225], v[176:177] op_sel:[0,1,0]
	s_nop 0
	v_pk_fma_f32 v[172:173], v[128:129], v[226:227], v[172:173] op_sel_hi:[1,0,1]
	v_mov_b32_e32 v174, v227
	v_pk_fma_f32 v[176:177], v[130:131], v[174:175], v[172:173] op_sel_hi:[1,0,1]
	ds_read_b128 v[240:243], v244 offset:20480
	s_waitcnt lgkmcnt(3)
	v_pk_fma_f32 v[176:177], v[112:113], v[228:229], v[176:177] op_sel_hi:[1,0,1]
	s_nop 0
	v_pk_fma_f32 v[172:173], v[114:115], v[228:229], v[176:177] op_sel:[0,1,0]
	s_nop 0
	v_pk_fma_f32 v[172:173], v[118:119], v[230:231], v[172:173] op_sel_hi:[1,0,1]
	v_mov_b32_e32 v174, v231
	v_pk_fma_f32 v[176:177], v[122:123], v[174:175], v[172:173] op_sel_hi:[1,0,1]
	ds_read_b128 v[224:227], v244 offset:21504
	s_waitcnt lgkmcnt(3)
	v_pk_fma_f32 v[176:177], v[108:109], v[232:233], v[176:177] op_sel_hi:[1,0,1]
	s_nop 0
	v_pk_fma_f32 v[172:173], v[110:111], v[232:233], v[176:177] op_sel:[0,1,0]
	s_nop 0
	v_pk_fma_f32 v[172:173], v[116:117], v[234:235], v[172:173] op_sel_hi:[1,0,1]
	v_mov_b32_e32 v174, v235
	v_pk_fma_f32 v[176:177], v[120:121], v[174:175], v[172:173] op_sel_hi:[1,0,1]
	ds_read_b128 v[228:231], v244 offset:22528
	s_waitcnt lgkmcnt(3)
	v_pk_fma_f32 v[176:177], v[96:97], v[236:237], v[176:177] op_sel_hi:[1,0,1]
	s_nop 0
	v_pk_fma_f32 v[172:173], v[98:99], v[236:237], v[176:177] op_sel:[0,1,0]
	s_nop 0
	v_pk_fma_f32 v[172:173], v[102:103], v[238:239], v[172:173] op_sel_hi:[1,0,1]
	v_mov_b32_e32 v174, v239
	v_pk_fma_f32 v[176:177], v[106:107], v[174:175], v[172:173] op_sel_hi:[1,0,1]
	ds_read_b128 v[232:235], v244 offset:23552
	s_waitcnt lgkmcnt(3)
	v_pk_fma_f32 v[176:177], v[92:93], v[240:241], v[176:177] op_sel_hi:[1,0,1]
	s_nop 0
	v_pk_fma_f32 v[172:173], v[94:95], v[240:241], v[176:177] op_sel:[0,1,0]
	s_nop 0
	v_pk_fma_f32 v[172:173], v[100:101], v[242:243], v[172:173] op_sel_hi:[1,0,1]
	v_mov_b32_e32 v174, v243
	v_pk_fma_f32 v[176:177], v[104:105], v[174:175], v[172:173] op_sel_hi:[1,0,1]
	ds_read_b128 v[236:239], v244 offset:24576
	s_waitcnt lgkmcnt(3)
	v_pk_fma_f32 v[176:177], v[80:81], v[224:225], v[176:177] op_sel_hi:[1,0,1]
	s_nop 0
	v_pk_fma_f32 v[172:173], v[82:83], v[224:225], v[176:177] op_sel:[0,1,0]
	s_nop 0
	v_pk_fma_f32 v[172:173], v[86:87], v[226:227], v[172:173] op_sel_hi:[1,0,1]
	v_mov_b32_e32 v174, v227
	v_pk_fma_f32 v[176:177], v[90:91], v[174:175], v[172:173] op_sel_hi:[1,0,1]
	ds_read_b128 v[240:243], v244 offset:25600
	s_waitcnt lgkmcnt(3)
	v_pk_fma_f32 v[176:177], v[76:77], v[228:229], v[176:177] op_sel_hi:[1,0,1]
	s_nop 0
	v_pk_fma_f32 v[172:173], v[78:79], v[228:229], v[176:177] op_sel:[0,1,0]
	s_nop 0
	v_pk_fma_f32 v[172:173], v[84:85], v[230:231], v[172:173] op_sel_hi:[1,0,1]
	v_mov_b32_e32 v174, v231
	v_pk_fma_f32 v[176:177], v[88:89], v[174:175], v[172:173] op_sel_hi:[1,0,1]
	ds_read_b128 v[224:227], v244 offset:26624
	s_waitcnt lgkmcnt(3)
	v_pk_fma_f32 v[176:177], v[68:69], v[232:233], v[176:177] op_sel_hi:[1,0,1]
	s_nop 0
	v_pk_fma_f32 v[172:173], v[70:71], v[232:233], v[176:177] op_sel:[0,1,0]
	s_nop 0
	v_pk_fma_f32 v[172:173], v[72:73], v[234:235], v[172:173] op_sel_hi:[1,0,1]
	v_mov_b32_e32 v174, v235
	v_pk_fma_f32 v[172:173], v[74:75], v[174:175], v[172:173] op_sel_hi:[1,0,1]
	ds_read_b128 v[228:231], v244 offset:27648
	s_waitcnt lgkmcnt(3)
	v_pk_fma_f32 v[178:179], v[124:125], v[236:237], 0 op_sel_hi:[1,0,0]
	s_nop 0
	v_pk_fma_f32 v[174:175], v[126:127], v[236:237], v[178:179] op_sel:[0,1,0]
	s_nop 0
	v_pk_fma_f32 v[174:175], v[128:129], v[238:239], v[174:175] op_sel_hi:[1,0,1]
	v_mov_b32_e32 v176, v239
	v_pk_fma_f32 v[178:179], v[130:131], v[176:177], v[174:175] op_sel_hi:[1,0,1]
	ds_read_b128 v[232:235], v244 offset:28672
	s_waitcnt lgkmcnt(3)
; #define LAS __attribute__((address_space(3)))
; __device__ __forceinline__ void phase_norm2(const Params& p, const Ctx& F, const int l) {
;     ...
; #pragma unroll
;         for (int e = 0; e < 16; ++e) { f32x2 a = {0.f, 0.f};
; #pragma unroll
;             for (int j = 0; j < 8; ++j) { const f32x4 w = *((const LAS f32x4*)(wr2 + e * DM) + F.lane + 64 * j);
; #pragma unroll
;                 for (int c = 0; c < 4; ++c) a += vv[j][c] * w[c]; }
;             lg[e] = a; }
	v_pk_fma_f32 v[178:179], v[112:113], v[240:241], v[178:179] op_sel_hi:[1,0,1]
	s_nop 0
	v_pk_fma_f32 v[174:175], v[114:115], v[240:241], v[178:179] op_sel:[0,1,0]
	s_nop 0
	v_pk_fma_f32 v[174:175], v[118:119], v[242:243], v[174:175] op_sel_hi:[1,0,1]
	v_mov_b32_e32 v176, v243
	v_pk_fma_f32 v[178:179], v[122:123], v[176:177], v[174:175] op_sel_hi:[1,0,1]
	ds_read_b128 v[236:239], v244 offset:29696
	s_waitcnt lgkmcnt(3)
	v_pk_fma_f32 v[178:179], v[108:109], v[224:225], v[178:179] op_sel_hi:[1,0,1]
	s_nop 0
	v_pk_fma_f32 v[174:175], v[110:111], v[224:225], v[178:179] op_sel:[0,1,0]
	s_nop 0
	v_pk_fma_f32 v[174:175], v[116:117], v[226:227], v[174:175] op_sel_hi:[1,0,1]
	v_mov_b32_e32 v176, v227
	v_pk_fma_f32 v[178:179], v[120:121], v[176:177], v[174:175] op_sel_hi:[1,0,1]
	ds_read_b128 v[240:243], v244 offset:30720
	s_waitcnt lgkmcnt(3)
	v_pk_fma_f32 v[178:179], v[96:97], v[228:229], v[178:179] op_sel_hi:[1,0,1]
	s_nop 0
	v_pk_fma_f32 v[174:175], v[98:99], v[228:229], v[178:179] op_sel:[0,1,0]
	s_nop 0
	v_pk_fma_f32 v[174:175], v[102:103], v[230:231], v[174:175] op_sel_hi:[1,0,1]
	v_mov_b32_e32 v176, v231
	v_pk_fma_f32 v[178:179], v[106:107], v[176:177], v[174:175] op_sel_hi:[1,0,1]
	ds_read_b128 v[224:227], v244 offset:31744
	s_waitcnt lgkmcnt(3)
	v_pk_fma_f32 v[178:179], v[92:93], v[232:233], v[178:179] op_sel_hi:[1,0,1]
	s_nop 0
	v_pk_fma_f32 v[174:175], v[94:95], v[232:233], v[178:179] op_sel:[0,1,0]
	s_nop 0
	v_pk_fma_f32 v[174:175], v[100:101], v[234:235], v[174:175] op_sel_hi:[1,0,1]
	v_mov_b32_e32 v176, v235
	v_pk_fma_f32 v[178:179], v[104:105], v[176:177], v[174:175] op_sel_hi:[1,0,1]
	ds_read_b128 v[228:231], v244 offset:32768
	s_waitcnt lgkmcnt(3)
	v_pk_fma_f32 v[178:179], v[80:81], v[236:237], v[178:179] op_sel_hi:[1,0,1]
	s_nop 0
	v_pk_fma_f32 v[174:175], v[82:83], v[236:237], v[178:179] op_sel:[0,1,0]
	s_nop 0
	v_pk_fma_f32 v[174:175], v[86:87], v[238:239], v[174:175] op_sel_hi:[1,0,1]
	v_mov_b32_e32 v176, v239
	v_pk_fma_f32 v[178:179], v[90:91], v[176:177], v[174:175] op_sel_hi:[1,0,1]
	ds_read_b128 v[232:235], v244 offset:33792
	s_waitcnt lgkmcnt(3)
	v_pk_fma_f32 v[178:179], v[76:77], v[240:241], v[178:179] op_sel_hi:[1,0,1]
	s_nop 0
	v_pk_fma_f32 v[174:175], v[78:79], v[240:241], v[178:179] op_sel:[0,1,0]
	s_nop 0
	v_pk_fma_f32 v[174:175], v[84:85], v[242:243], v[174:175] op_sel_hi:[1,0,1]
	v_mov_b32_e32 v176, v243
	v_pk_fma_f32 v[178:179], v[88:89], v[176:177], v[174:175] op_sel_hi:[1,0,1]
	ds_read_b128 v[236:239], v244 offset:34816
	s_waitcnt lgkmcnt(3)
	v_pk_fma_f32 v[178:179], v[68:69], v[224:225], v[178:179] op_sel_hi:[1,0,1]
	s_nop 0
	v_pk_fma_f32 v[174:175], v[70:71], v[224:225], v[178:179] op_sel:[0,1,0]
	s_nop 0
	v_pk_fma_f32 v[174:175], v[72:73], v[226:227], v[174:175] op_sel_hi:[1,0,1]
	v_mov_b32_e32 v176, v227
	v_pk_fma_f32 v[174:175], v[74:75], v[176:177], v[174:175] op_sel_hi:[1,0,1]
	ds_read_b128 v[240:243], v244 offset:35840
	s_waitcnt lgkmcnt(3)
	v_pk_fma_f32 v[180:181], v[124:125], v[228:229], 0 op_sel_hi:[1,0,0]
	s_nop 0
	v_pk_fma_f32 v[176:177], v[126:127], v[228:229], v[180:181] op_sel:[0,1,0]
	s_nop 0
	v_pk_fma_f32 v[176:177], v[128:129], v[230:231], v[176:177] op_sel_hi:[1,0,1]
	v_mov_b32_e32 v178, v231
	v_pk_fma_f32 v[180:181], v[130:131], v[178:179], v[176:177] op_sel_hi:[1,0,1]
	ds_read_b128 v[224:227], v244 offset:36864
	s_waitcnt lgkmcnt(3)
	v_pk_fma_f32 v[180:181], v[112:113], v[232:233], v[180:181] op_sel_hi:[1,0,1]
	s_nop 0
	v_pk_fma_f32 v[176:177], v[114:115], v[232:233], v[180:181] op_sel:[0,1,0]
	s_nop 0
	v_pk_fma_f32 v[176:177], v[118:119], v[234:235], v[176:177] op_sel_hi:[1,0,1]
	v_mov_b32_e32 v178, v235
	v_pk_fma_f32 v[180:181], v[122:123], v[178:179], v[176:177] op_sel_hi:[1,0,1]
	ds_read_b128 v[228:231], v244 offset:37888
	s_waitcnt lgkmcnt(3)
	v_pk_fma_f32 v[180:181], v[108:109], v[236:237], v[180:181] op_sel_hi:[1,0,1]
	s_nop 0
	v_pk_fma_f32 v[176:177], v[110:111], v[236:237], v[180:181] op_sel:[0,1,0]
	s_nop 0
	v_pk_fma_f32 v[176:177], v[116:117], v[238:239], v[176:177] op_sel_hi:[1,0,1]
	v_mov_b32_e32 v178, v239
	v_pk_fma_f32 v[180:181], v[120:121], v[178:179], v[176:177] op_sel_hi:[1,0,1]
	ds_read_b128 v[232:235], v244 offset:38912
	s_waitcnt lgkmcnt(3)
	v_pk_fma_f32 v[180:181], v[96:97], v[240:241], v[180:181] op_sel_hi:[1,0,1]
	s_nop 0
	v_pk_fma_f32 v[176:177], v[98:99], v[240:241], v[180:181] op_sel:[0,1,0]
	s_nop 0
	v_pk_fma_f32 v[176:177], v[102:103], v[242:243], v[176:177] op_sel_hi:[1,0,1]
	v_mov_b32_e32 v178, v243
	v_pk_fma_f32 v[180:181], v[106:107], v[178:179], v[176:177] op_sel_hi:[1,0,1]
	ds_read_b128 v[236:239], v244 offset:39936
	s_waitcnt lgkmcnt(3)
	v_pk_fma_f32 v[180:181], v[92:93], v[224:225], v[180:181] op_sel_hi:[1,0,1]
	s_nop 0
	v_pk_fma_f32 v[176:177], v[94:95], v[224:225], v[180:181] op_sel:[0,1,0]
	s_nop 0
	v_pk_fma_f32 v[176:177], v[100:101], v[226:227], v[176:177] op_sel_hi:[1,0,1]
	v_mov_b32_e32 v178, v227
	v_pk_fma_f32 v[180:181], v[104:105], v[178:179], v[176:177] op_sel_hi:[1,0,1]
	ds_read_b128 v[240:243], v244 offset:40960
	s_waitcnt lgkmcnt(3)
	v_pk_fma_f32 v[180:181], v[80:81], v[228:229], v[180:181] op_sel_hi:[1,0,1]
	s_nop 0
	v_pk_fma_f32 v[176:177], v[82:83], v[228:229], v[180:181] op_sel:[0,1,0]
	s_nop 0
	v_pk_fma_f32 v[176:177], v[86:87], v[230:231], v[176:177] op_sel_hi:[1,0,1]
	v_mov_b32_e32 v178, v231
	v_pk_fma_f32 v[180:181], v[90:91], v[178:179], v[176:177] op_sel_hi:[1,0,1]
	ds_read_b128 v[224:227], v244 offset:41984
	s_waitcnt lgkmcnt(3)
; #define LAS __attribute__((address_space(3)))
; __device__ __forceinline__ void phase_norm2(const Params& p, const Ctx& F, const int l) {
;     ...
; #pragma unroll
;         for (int e = 0; e < 16; ++e) { f32x2 a = {0.f, 0.f};
; #pragma unroll
;             for (int j = 0; j < 8; ++j) { const f32x4 w = *((const LAS f32x4*)(wr2 + e * DM) + F.lane + 64 * j);
; #pragma unroll
;                 for (int c = 0; c < 4; ++c) a += vv[j][c] * w[c]; }
;             lg[e] = a; }
	v_pk_fma_f32 v[180:181], v[76:77], v[232:233], v[180:181] op_sel_hi:[1,0,1]
	s_nop 0
	v_pk_fma_f32 v[176:177], v[78:79], v[232:233], v[180:181] op_sel:[0,1,0]
	s_nop 0
	v_pk_fma_f32 v[176:177], v[84:85], v[234:235], v[176:177] op_sel_hi:[1,0,1]
	v_mov_b32_e32 v178, v235
	v_pk_fma_f32 v[180:181], v[88:89], v[178:179], v[176:177] op_sel_hi:[1,0,1]
	ds_read_b128 v[228:231], v244 offset:43008
	s_waitcnt lgkmcnt(3)
	v_pk_fma_f32 v[180:181], v[68:69], v[236:237], v[180:181] op_sel_hi:[1,0,1]
	s_nop 0
	v_pk_fma_f32 v[176:177], v[70:71], v[236:237], v[180:181] op_sel:[0,1,0]
	s_nop 0
	v_pk_fma_f32 v[176:177], v[72:73], v[238:239], v[176:177] op_sel_hi:[1,0,1]
	v_mov_b32_e32 v178, v239
	v_pk_fma_f32 v[176:177], v[74:75], v[178:179], v[176:177] op_sel_hi:[1,0,1]
	ds_read_b128 v[232:235], v244 offset:44032
	s_waitcnt lgkmcnt(3)
	v_pk_fma_f32 v[184:185], v[124:125], v[240:241], 0 op_sel_hi:[1,0,0]
	s_nop 0
	v_pk_fma_f32 v[178:179], v[126:127], v[240:241], v[184:185] op_sel:[0,1,0]
	s_nop 0
	v_pk_fma_f32 v[178:179], v[128:129], v[242:243], v[178:179] op_sel_hi:[1,0,1]
	v_mov_b32_e32 v180, v243
	v_pk_fma_f32 v[184:185], v[130:131], v[180:181], v[178:179] op_sel_hi:[1,0,1]
	ds_read_b128 v[236:239], v244 offset:45056
	s_waitcnt lgkmcnt(3)
	v_pk_fma_f32 v[184:185], v[112:113], v[224:225], v[184:185] op_sel_hi:[1,0,1]
	s_nop 0
	v_pk_fma_f32 v[178:179], v[114:115], v[224:225], v[184:185] op_sel:[0,1,0]
	s_nop 0
	v_pk_fma_f32 v[178:179], v[118:119], v[226:227], v[178:179] op_sel_hi:[1,0,1]
	v_mov_b32_e32 v180, v227
	v_pk_fma_f32 v[184:185], v[122:123], v[180:181], v[178:179] op_sel_hi:[1,0,1]
	ds_read_b128 v[240:243], v244 offset:46080
	s_waitcnt lgkmcnt(3)
	v_pk_fma_f32 v[184:185], v[108:109], v[228:229], v[184:185] op_sel_hi:[1,0,1]
	s_nop 0
	v_pk_fma_f32 v[178:179], v[110:111], v[228:229], v[184:185] op_sel:[0,1,0]
	s_nop 0
	v_pk_fma_f32 v[178:179], v[116:117], v[230:231], v[178:179] op_sel_hi:[1,0,1]
	v_mov_b32_e32 v180, v231
	v_pk_fma_f32 v[184:185], v[120:121], v[180:181], v[178:179] op_sel_hi:[1,0,1]
	ds_read_b128 v[224:227], v244 offset:47104
	s_waitcnt lgkmcnt(3)
	v_pk_fma_f32 v[184:185], v[96:97], v[232:233], v[184:185] op_sel_hi:[1,0,1]
	s_nop 0
	v_pk_fma_f32 v[178:179], v[98:99], v[232:233], v[184:185] op_sel:[0,1,0]
	s_nop 0
	v_pk_fma_f32 v[178:179], v[102:103], v[234:235], v[178:179] op_sel_hi:[1,0,1]
	v_mov_b32_e32 v180, v235
	v_pk_fma_f32 v[184:185], v[106:107], v[180:181], v[178:179] op_sel_hi:[1,0,1]
	ds_read_b128 v[228:231], v244 offset:48128
	s_waitcnt lgkmcnt(3)
	v_pk_fma_f32 v[184:185], v[92:93], v[236:237], v[184:185] op_sel_hi:[1,0,1]
	s_nop 0
	v_pk_fma_f32 v[178:179], v[94:95], v[236:237], v[184:185] op_sel:[0,1,0]
	s_nop 0
	v_pk_fma_f32 v[178:179], v[100:101], v[238:239], v[178:179] op_sel_hi:[1,0,1]
	v_mov_b32_e32 v180, v239
	v_pk_fma_f32 v[184:185], v[104:105], v[180:181], v[178:179] op_sel_hi:[1,0,1]
	ds_read_b128 v[232:235], v244 offset:49152
	s_waitcnt lgkmcnt(3)
	v_pk_fma_f32 v[184:185], v[80:81], v[240:241], v[184:185] op_sel_hi:[1,0,1]
	s_nop 0
	v_pk_fma_f32 v[178:179], v[82:83], v[240:241], v[184:185] op_sel:[0,1,0]
	s_nop 0
	v_pk_fma_f32 v[178:179], v[86:87], v[242:243], v[178:179] op_sel_hi:[1,0,1]
	v_mov_b32_e32 v180, v243
	v_pk_fma_f32 v[184:185], v[90:91], v[180:181], v[178:179] op_sel_hi:[1,0,1]
	ds_read_b128 v[236:239], v244 offset:50176
	s_waitcnt lgkmcnt(3)
	v_pk_fma_f32 v[184:185], v[76:77], v[224:225], v[184:185] op_sel_hi:[1,0,1]
	s_nop 0
	v_pk_fma_f32 v[178:179], v[78:79], v[224:225], v[184:185] op_sel:[0,1,0]
	s_nop 0
	v_pk_fma_f32 v[178:179], v[84:85], v[226:227], v[178:179] op_sel_hi:[1,0,1]
	v_mov_b32_e32 v180, v227
	v_pk_fma_f32 v[184:185], v[88:89], v[180:181], v[178:179] op_sel_hi:[1,0,1]
	ds_read_b128 v[240:243], v244 offset:51200
	s_waitcnt lgkmcnt(3)
	v_pk_fma_f32 v[184:185], v[68:69], v[228:229], v[184:185] op_sel_hi:[1,0,1]
	s_nop 0
	v_pk_fma_f32 v[178:179], v[70:71], v[228:229], v[184:185] op_sel:[0,1,0]
	ds_read_b128 v[224:227], v244 offset:52224
	v_pk_fma_f32 v[178:179], v[72:73], v[230:231], v[178:179] op_sel_hi:[1,0,1]
	v_mov_b32_e32 v180, v231
	v_pk_fma_f32 v[178:179], v[74:75], v[180:181], v[178:179] op_sel_hi:[1,0,1]
	s_waitcnt lgkmcnt(3)
	v_pk_fma_f32 v[180:181], v[124:125], v[232:233], 0 op_sel_hi:[1,0,0]
	s_nop 0
	v_pk_fma_f32 v[180:181], v[126:127], v[232:233], v[180:181] op_sel:[0,1,0]
	v_mov_b32_e32 v184, v235
	v_pk_fma_f32 v[180:181], v[128:129], v[234:235], v[180:181] op_sel_hi:[1,0,1]
	s_nop 0
	v_pk_fma_f32 v[180:181], v[130:131], v[184:185], v[180:181] op_sel_hi:[1,0,1]
	ds_read_b128 v[228:231], v244 offset:53248
	s_waitcnt lgkmcnt(3)
	v_pk_fma_f32 v[180:181], v[112:113], v[236:237], v[180:181] op_sel_hi:[1,0,1]
	s_nop 0
	v_pk_fma_f32 v[180:181], v[114:115], v[236:237], v[180:181] op_sel:[0,1,0]
	v_mov_b32_e32 v184, v239
	v_pk_fma_f32 v[180:181], v[118:119], v[238:239], v[180:181] op_sel_hi:[1,0,1]
	s_nop 0
	v_pk_fma_f32 v[180:181], v[122:123], v[184:185], v[180:181] op_sel_hi:[1,0,1]
	ds_read_b128 v[232:235], v244 offset:54272
	s_waitcnt lgkmcnt(3)
	v_pk_fma_f32 v[180:181], v[108:109], v[240:241], v[180:181] op_sel_hi:[1,0,1]
	s_nop 0
	v_pk_fma_f32 v[180:181], v[110:111], v[240:241], v[180:181] op_sel:[0,1,0]
	v_mov_b32_e32 v184, v243
	v_pk_fma_f32 v[180:181], v[116:117], v[242:243], v[180:181] op_sel_hi:[1,0,1]
	s_nop 0
	v_pk_fma_f32 v[180:181], v[120:121], v[184:185], v[180:181] op_sel_hi:[1,0,1]
	ds_read_b128 v[236:239], v244 offset:55296
	s_waitcnt lgkmcnt(3)
	v_pk_fma_f32 v[180:181], v[96:97], v[224:225], v[180:181] op_sel_hi:[1,0,1]
	s_nop 0
	v_pk_fma_f32 v[180:181], v[98:99], v[224:225], v[180:181] op_sel:[0,1,0]
	v_mov_b32_e32 v184, v227
	v_pk_fma_f32 v[180:181], v[102:103], v[226:227], v[180:181] op_sel_hi:[1,0,1]
	s_nop 0
	v_pk_fma_f32 v[180:181], v[106:107], v[184:185], v[180:181] op_sel_hi:[1,0,1]
	ds_read_b128 v[240:243], v244 offset:56320
	s_waitcnt lgkmcnt(3)
; #define LAS __attribute__((address_space(3)))
; __device__ __forceinline__ void phase_norm2(const Params& p, const Ctx& F, const int l) {
;     ...
; #pragma unroll
;         for (int e = 0; e < 16; ++e) { f32x2 a = {0.f, 0.f};
; #pragma unroll
;             for (int j = 0; j < 8; ++j) { const f32x4 w = *((const LAS f32x4*)(wr2 + e * DM) + F.lane + 64 * j);
; #pragma unroll
;                 for (int c = 0; c < 4; ++c) a += vv[j][c] * w[c]; }
;             lg[e] = a; }
;         float lg0[16], lg1[16];
; #pragma unroll
;         for (int e = 0; e < 16; ++e) { lg0[e] = lg[e].x; lg1[e] = lg[e].y; }
	v_pk_fma_f32 v[180:181], v[92:93], v[228:229], v[180:181] op_sel_hi:[1,0,1]
	s_nop 0
	v_pk_fma_f32 v[180:181], v[94:95], v[228:229], v[180:181] op_sel:[0,1,0]
	v_mov_b32_e32 v184, v231
	v_pk_fma_f32 v[180:181], v[100:101], v[230:231], v[180:181] op_sel_hi:[1,0,1]
	s_nop 0
	v_pk_fma_f32 v[180:181], v[104:105], v[184:185], v[180:181] op_sel_hi:[1,0,1]
	ds_read_b128 v[224:227], v244 offset:57344
	s_waitcnt lgkmcnt(3)
	v_pk_fma_f32 v[180:181], v[80:81], v[232:233], v[180:181] op_sel_hi:[1,0,1]
	s_nop 0
	v_pk_fma_f32 v[180:181], v[82:83], v[232:233], v[180:181] op_sel:[0,1,0]
	v_mov_b32_e32 v184, v235
	v_pk_fma_f32 v[180:181], v[86:87], v[234:235], v[180:181] op_sel_hi:[1,0,1]
	s_nop 0
	v_pk_fma_f32 v[180:181], v[90:91], v[184:185], v[180:181] op_sel_hi:[1,0,1]
	ds_read_b128 v[228:231], v244 offset:58368
	s_waitcnt lgkmcnt(3)
	v_pk_fma_f32 v[180:181], v[76:77], v[236:237], v[180:181] op_sel_hi:[1,0,1]
	s_nop 0
	v_pk_fma_f32 v[180:181], v[78:79], v[236:237], v[180:181] op_sel:[0,1,0]
	v_mov_b32_e32 v184, v239
	v_pk_fma_f32 v[180:181], v[84:85], v[238:239], v[180:181] op_sel_hi:[1,0,1]
	s_nop 0
	v_pk_fma_f32 v[180:181], v[88:89], v[184:185], v[180:181] op_sel_hi:[1,0,1]
	ds_read_b128 v[232:235], v244 offset:59392
	s_waitcnt lgkmcnt(3)
	v_pk_fma_f32 v[180:181], v[68:69], v[240:241], v[180:181] op_sel_hi:[1,0,1]
	s_nop 0
	v_pk_fma_f32 v[180:181], v[70:71], v[240:241], v[180:181] op_sel:[0,1,0]
	v_mov_b32_e32 v184, v243
	v_pk_fma_f32 v[180:181], v[72:73], v[242:243], v[180:181] op_sel_hi:[1,0,1]
	s_nop 0
	v_pk_fma_f32 v[180:181], v[74:75], v[184:185], v[180:181] op_sel_hi:[1,0,1]
	ds_read_b128 v[236:239], v244 offset:60416
	s_waitcnt lgkmcnt(3)
	v_pk_fma_f32 v[124:125], v[124:125], v[224:225], 0 op_sel_hi:[1,0,0]
	s_nop 0
	v_pk_fma_f32 v[124:125], v[126:127], v[224:225], v[124:125] op_sel:[0,1,0]
	v_mov_b32_e32 v126, v227
	v_pk_fma_f32 v[124:125], v[128:129], v[226:227], v[124:125] op_sel_hi:[1,0,1]
	s_nop 0
	v_pk_fma_f32 v[128:129], v[130:131], v[126:127], v[124:125] op_sel_hi:[1,0,1]
	ds_read_b128 v[240:243], v244 offset:61440
	s_waitcnt lgkmcnt(3)
	v_pk_fma_f32 v[112:113], v[112:113], v[228:229], v[128:129] op_sel_hi:[1,0,1]
	s_nop 0
	v_pk_fma_f32 v[112:113], v[114:115], v[228:229], v[112:113] op_sel:[0,1,0]
	v_mov_b32_e32 v114, v231
	v_pk_fma_f32 v[112:113], v[118:119], v[230:231], v[112:113] op_sel_hi:[1,0,1]
	s_nop 0
	v_pk_fma_f32 v[118:119], v[122:123], v[114:115], v[112:113] op_sel_hi:[1,0,1]
	ds_read_b128 v[224:227], v244 offset:62464
	s_waitcnt lgkmcnt(3)
	v_pk_fma_f32 v[108:109], v[108:109], v[232:233], v[118:119] op_sel_hi:[1,0,1]
	s_nop 0
	v_pk_fma_f32 v[108:109], v[110:111], v[232:233], v[108:109] op_sel:[0,1,0]
	v_mov_b32_e32 v110, v235
	v_pk_fma_f32 v[108:109], v[116:117], v[234:235], v[108:109] op_sel_hi:[1,0,1]
	s_nop 0
	v_pk_fma_f32 v[112:113], v[120:121], v[110:111], v[108:109] op_sel_hi:[1,0,1]
	ds_read_b128 v[228:231], v244 offset:63488
	s_waitcnt lgkmcnt(3)
	v_pk_fma_f32 v[96:97], v[96:97], v[236:237], v[112:113] op_sel_hi:[1,0,1]
	s_nop 0
	v_pk_fma_f32 v[96:97], v[98:99], v[236:237], v[96:97] op_sel:[0,1,0]
	v_mov_b32_e32 v98, v239
	v_pk_fma_f32 v[96:97], v[102:103], v[238:239], v[96:97] op_sel_hi:[1,0,1]
	s_nop 0
	v_pk_fma_f32 v[102:103], v[106:107], v[98:99], v[96:97] op_sel_hi:[1,0,1]
	ds_read_b128 v[232:235], v244 offset:64512
	s_waitcnt lgkmcnt(3)
	v_pk_fma_f32 v[92:93], v[92:93], v[240:241], v[102:103] op_sel_hi:[1,0,1]
	s_nop 0
	v_pk_fma_f32 v[92:93], v[94:95], v[240:241], v[92:93] op_sel:[0,1,0]
	v_mov_b32_e32 v94, v243
	v_pk_fma_f32 v[92:93], v[100:101], v[242:243], v[92:93] op_sel_hi:[1,0,1]
	s_nop 0
	v_pk_fma_f32 v[96:97], v[104:105], v[94:95], v[92:93] op_sel_hi:[1,0,1]
	s_waitcnt lgkmcnt(2)
	v_pk_fma_f32 v[80:81], v[80:81], v[224:225], v[96:97] op_sel_hi:[1,0,1]
	s_nop 0
	v_pk_fma_f32 v[80:81], v[82:83], v[224:225], v[80:81] op_sel:[0,1,0]
	v_mov_b32_e32 v82, v227
	v_pk_fma_f32 v[80:81], v[86:87], v[226:227], v[80:81] op_sel_hi:[1,0,1]
	s_nop 0
	v_pk_fma_f32 v[86:87], v[90:91], v[82:83], v[80:81] op_sel_hi:[1,0,1]
	s_waitcnt lgkmcnt(1)
	v_pk_fma_f32 v[76:77], v[76:77], v[228:229], v[86:87] op_sel_hi:[1,0,1]
	s_nop 0
	v_pk_fma_f32 v[76:77], v[78:79], v[228:229], v[76:77] op_sel:[0,1,0]
	v_mov_b32_e32 v78, v231
	v_pk_fma_f32 v[76:77], v[84:85], v[230:231], v[76:77] op_sel_hi:[1,0,1]
	s_nop 0
	v_pk_fma_f32 v[80:81], v[88:89], v[78:79], v[76:77] op_sel_hi:[1,0,1]
	v_cndmask_b32_e64 v1, v168, v152, s[38:39]
	s_waitcnt lgkmcnt(0)
; __device__ __forceinline__ void router_tail(const Ctx& F, const float (&lg)[16], const int b, const int t, const bool valid) {
;     const bool b5 = (F.lane & 32) != 0, b4 = (F.lane & 16) != 0, b3 = (F.lane & 8) != 0, b2 = (F.lane & 4) != 0;
;     float r8[8], r4[4], r2[2];
; #pragma unroll
;     for (int e = 0; e < 8; ++e) { const float keep = b5 ? lg[e + 8] : lg[e], send = b5 ? lg[e] : lg[e + 8]; r8[e] = keep + __shfl_xor(send, 32); }
; #pragma unroll
;     for (int e = 0; e < 4; ++e) { const float keep = b4 ? r8[e + 4] : r8[e], send = b4 ? r8[e] : r8[e + 4]; r4[e] = keep + __shfl_xor(send, 16); }
; #pragma unroll
;     for (int e = 0; e < 2; ++e) { const float keep = b3 ? r4[e + 2] : r4[e], send = b3 ? r4[e] : r4[e + 2]; r2[e] = keep + __shfl_xor(send, 8); }
;     float lgt; { const float keep = b2 ? r2[1] : r2[0], send = b2 ? r2[0] : r2[1]; lgt = keep + __shfl_xor(send, 4); }
;     lgt += __shfl_xor(lgt, 2); lgt += __shfl_xor(lgt, 1);
;     float mx = lgt;
;     mx = fmaxf(mx, __shfl_xor(mx, 4)); mx = fmaxf(mx, __shfl_xor(mx, 8)); mx = fmaxf(mx, __shfl_xor(mx, 16)); mx = fmaxf(mx, __shfl_xor(mx, 32));
;     const float ex = expf(lgt - mx); float sum = ex;
;     sum += __shfl_xor(sum, 4); sum += __shfl_xor(sum, 8); sum += __shfl_xor(sum, 16); sum += __shfl_xor(sum, 32);
;     if (valid && (F.lane & 3) == 0) { const float af = ex / sum; const int e = F.lane >> 2;
;         if (t < CTXL) F.affc[((size_t)(b * 16 + e)) * CTXL + t] = af; else F.affl[((size_t)(b * 16 + e)) * SEQ + (t - CTXL)] = af; }
	v_pk_fma_f32 v[68:69], v[68:69], v[232:233], v[80:81] op_sel_hi:[1,0,1]
	s_nop 0
	v_pk_fma_f32 v[68:69], v[70:71], v[232:233], v[68:69] op_sel:[0,1,0]
	v_mov_b32_e32 v70, v235
	v_pk_fma_f32 v[68:69], v[72:73], v[234:235], v[68:69] op_sel_hi:[1,0,1]
	v_cndmask_b32_e64 v72, v156, v172, s[38:39]
	v_pk_fma_f32 v[68:69], v[74:75], v[70:71], v[68:69] op_sel_hi:[1,0,1]
	v_cndmask_b32_e64 v70, v152, v168, s[38:39]
	ds_bpermute_b32 v70, v194, v70
	v_cndmask_b32_e64 v71, v154, v170, s[38:39]
	ds_bpermute_b32 v71, v194, v71
	ds_bpermute_b32 v72, v194, v72
	v_cndmask_b32_e64 v73, v158, v174, s[38:39]
	ds_bpermute_b32 v73, v194, v73
	v_cndmask_b32_e64 v74, v160, v176, s[38:39]
	ds_bpermute_b32 v74, v194, v74
	v_cndmask_b32_e64 v75, v162, v178, s[38:39]
	s_waitcnt lgkmcnt(4)
	v_add_f32_e32 v1, v1, v70
	v_cndmask_b32_e64 v70, v170, v154, s[38:39]
	ds_bpermute_b32 v75, v194, v75
	v_cndmask_b32_e64 v76, v164, v180, s[38:39]
	s_waitcnt lgkmcnt(4)
	v_add_f32_e32 v70, v70, v71
	v_cndmask_b32_e64 v71, v172, v156, s[38:39]
	ds_bpermute_b32 v76, v194, v76
	s_waitcnt lgkmcnt(4)
	v_add_f32_e32 v71, v71, v72
	v_cndmask_b32_e64 v72, v174, v158, s[38:39]
	s_waitcnt lgkmcnt(3)
	v_add_f32_e32 v72, v72, v73
	v_cndmask_b32_e64 v73, v176, v160, s[38:39]
	s_waitcnt lgkmcnt(2)
	v_add_f32_e32 v73, v73, v74
	v_cndmask_b32_e64 v74, v178, v162, s[38:39]
	s_waitcnt lgkmcnt(1)
	v_add_f32_e32 v74, v74, v75
	v_cndmask_b32_e64 v75, v180, v164, s[38:39]
	s_waitcnt lgkmcnt(0)
	v_add_f32_e32 v75, v75, v76
	v_cndmask_b32_e64 v76, v68, v166, s[38:39]
	v_cndmask_b32_e64 v68, v166, v68, s[38:39]
	ds_bpermute_b32 v68, v194, v68
	s_waitcnt lgkmcnt(0)
	v_add_f32_e32 v68, v76, v68
	v_cndmask_b32_e64 v76, v73, v1, s[40:41]
	v_cndmask_b32_e64 v1, v1, v73, s[40:41]
	v_cndmask_b32_e64 v73, v74, v70, s[40:41]
	v_cndmask_b32_e64 v70, v70, v74, s[40:41]
	ds_bpermute_b32 v70, v193, v70
	ds_bpermute_b32 v1, v193, v1
	s_waitcnt lgkmcnt(1)
	v_add_f32_e32 v70, v73, v70
	v_cndmask_b32_e64 v73, v75, v71, s[40:41]
	v_cndmask_b32_e64 v71, v71, v75, s[40:41]
	ds_bpermute_b32 v71, v193, v71
	s_waitcnt lgkmcnt(1)
	v_add_f32_e32 v1, v76, v1
	s_waitcnt lgkmcnt(0)
	v_add_f32_e32 v71, v73, v71
	v_cndmask_b32_e64 v73, v68, v72, s[40:41]
	v_cndmask_b32_e64 v68, v72, v68, s[40:41]
	ds_bpermute_b32 v68, v193, v68
	v_cndmask_b32_e64 v72, v71, v1, s[42:43]
	v_cndmask_b32_e64 v1, v1, v71, s[42:43]
	ds_bpermute_b32 v1, v192, v1
	s_waitcnt lgkmcnt(1)
	v_add_f32_e32 v68, v73, v68
	v_cndmask_b32_e64 v71, v68, v70, s[42:43]
	v_cndmask_b32_e64 v68, v70, v68, s[42:43]
	ds_bpermute_b32 v68, v192, v68
	s_waitcnt lgkmcnt(1)
	v_add_f32_e32 v1, v72, v1
	s_waitcnt lgkmcnt(0)
	v_add_f32_e32 v68, v71, v68
	v_cndmask_b32_e64 v70, v68, v1, s[4:5]
	v_cndmask_b32_e64 v1, v1, v68, s[4:5]
	ds_bpermute_b32 v1, v191, v1
	s_waitcnt lgkmcnt(0)
	v_add_f32_e32 v1, v70, v1
	ds_bpermute_b32 v68, v190, v1
	s_waitcnt lgkmcnt(0)
	v_add_f32_e32 v1, v1, v68
	ds_bpermute_b32 v68, v133, v1
	s_waitcnt lgkmcnt(0)
	v_add_f32_e32 v1, v1, v68
	ds_bpermute_b32 v68, v191, v1
	s_waitcnt lgkmcnt(0)
	v_max_f32_e32 v68, v68, v68
	v_max_f32_e32 v68, v1, v68
	ds_bpermute_b32 v70, v192, v68
	s_waitcnt lgkmcnt(0)
	v_max_f32_e32 v70, v70, v70
	v_max_f32_e32 v68, v68, v70
	ds_bpermute_b32 v70, v193, v68
	s_waitcnt lgkmcnt(0)
	v_max_f32_e32 v70, v70, v70
	v_max_f32_e32 v68, v68, v70
	ds_bpermute_b32 v70, v194, v68
	s_waitcnt lgkmcnt(0)
	v_max_f32_e32 v70, v70, v70
	v_max_f32_e32 v68, v68, v70
	v_sub_f32_e32 v1, v1, v68
	v_mul_f32_e32 v68, 0x3fb8aa3b, v1
	v_fma_f32 v70, v1, s55, -v68
	v_rndne_f32_e32 v71, v68
	v_fmac_f32_e32 v70, 0x32a5705f, v1
	v_sub_f32_e32 v68, v68, v71
	v_add_f32_e32 v68, v68, v70
	v_exp_f32_e32 v68, v68
	v_cvt_i32_f32_e32 v70, v71
	v_cmp_ngt_f32_e32 vcc, s56, v1
	v_ldexp_f32 v68, v68, v70
	s_nop 0
	v_cndmask_b32_e32 v68, 0, v68, vcc
	v_cmp_nlt_f32_e32 vcc, s57, v1
	s_nop 1
	v_cndmask_b32_e32 v68, v222, v68, vcc
	ds_bpermute_b32 v1, v191, v68
	s_waitcnt lgkmcnt(0)
	v_add_f32_e32 v1, v68, v1
	ds_bpermute_b32 v70, v192, v1
	s_waitcnt lgkmcnt(0)
	v_add_f32_e32 v1, v1, v70
	ds_bpermute_b32 v70, v193, v1
	s_waitcnt lgkmcnt(0)
	v_add_f32_e32 v70, v1, v70
	ds_bpermute_b32 v71, v194, v70
	s_and_saveexec_b64 s[0:1], s[6:7]
	s_cbranch_execz .LBB0_942
	s_waitcnt lgkmcnt(0)
	v_add_f32_e32 v1, v70, v71
	v_div_scale_f32 v70, s[12:13], v1, v1, v68
	v_rcp_f32_e32 v71, v70
	v_div_scale_f32 v72, vcc, v68, v1, v68
	s_cmpk_gt_i32 s60, 0xff
	v_fma_f32 v73, -v70, v71, 1.0
	v_fmac_f32_e32 v71, v73, v71
	v_mul_f32_e32 v73, v72, v71
	v_fma_f32 v74, -v70, v73, v72
	v_fmac_f32_e32 v73, v74, v71
	v_fma_f32 v70, -v70, v73, v72
	v_div_fmas_f32 v70, v70, v71, v73
	v_div_fixup_f32 v68, v70, v1, v68
	s_mov_b64 s[12:13], -1
	s_cbranch_scc0 .LBB0_940
	v_lshl_add_u64 v[70:71], s[60:61], 2, v[148:149]
	global_store_dword v[70:71], v68, off offset:-1024
	s_mov_b64 s[12:13], 0
